# RG-LRU scan: the -log2e factor of the two gate sigmoids folded into one v_fmamk per element with pre-scaled biases (32 fewer VALU per 16-token tile)
# speedup vs baseline: 1.0104x; 1.0034x over previous
; #define LAS __attribute__((address_space(3)))
; __device__ __forceinline__ unsigned pk2(float lo, float hi) { const pk2_f32x2 v = {lo, hi}; return __builtin_bit_cast(unsigned, __builtin_convertvector(v, pk2_bf16x2)); }
; __device__ __forceinline__ void rec1_unit(KArgs args, int L, int unit, LAS unsigned char* lds, int wave, int lane) {
;     ...
;     for (int f = 0; f < 16; ++f) { const int mat = f >> 3, n = (f >> 1) & 3, kk = f & 1; const float* W = mat ? Wx : Wa;
;         const int jout = 8 * (fr >> 2) + (fr & 3) + 4 * (n & 1) + 32 * (n >> 1); const float* wp = W + (32 * kk + 8 * q) * 64 + jout;
;         u32x4 w; w.x = pk2(wp[0], wp[64]); w.y = pk2(wp[128], wp[192]); w.z = pk2(wp[256], wp[320]); w.w = pk2(wp[384], wp[448]);
;         *(LAS u32x4*)(wl + f * 1024 + lane * 16) = w; }
.LBB0_175:
	v_add_lshl_u32 v4, v145, v144, 2
	v_mov_b32_e32 v5, v0
	s_add_u32 s14, s8, s16
	s_addc_u32 s15, s9, s17
	s_add_u32 s0, s14, 0x2000
	s_addc_u32 s1, s15, 0
	v_lshl_add_u64 v[6:7], s[14:15], 0, v[4:5]
	v_lshl_add_u64 v[8:9], s[0:1], 0, v[4:5]
	global_load_dword v10, v[6:7], off
	global_load_dword v11, v[6:7], off offset:256
	global_load_dword v12, v[6:7], off offset:512
	global_load_dword v13, v[6:7], off offset:768
	global_load_dword v14, v[6:7], off offset:1024
	global_load_dword v15, v[6:7], off offset:1280
	global_load_dword v16, v[6:7], off offset:1536
	global_load_dword v17, v[6:7], off offset:1792
	global_load_dword v18, v[8:9], off
	global_load_dword v19, v[8:9], off offset:256
	global_load_dword v20, v[8:9], off offset:512
	global_load_dword v21, v[8:9], off offset:768
	global_load_dword v22, v[8:9], off offset:1024
	global_load_dword v23, v[8:9], off offset:1280
	global_load_dword v24, v[8:9], off offset:1536
	global_load_dword v25, v[8:9], off offset:1792
	global_load_dword v26, v[6:7], off offset:16
	global_load_dword v27, v[6:7], off offset:272
	global_load_dword v28, v[6:7], off offset:528
	global_load_dword v29, v[6:7], off offset:784
	global_load_dword v30, v[6:7], off offset:1040
	global_load_dword v31, v[6:7], off offset:1296
	global_load_dword v32, v[6:7], off offset:1552
	global_load_dword v33, v[6:7], off offset:1808
	global_load_dword v34, v[8:9], off offset:16
	global_load_dword v35, v[8:9], off offset:272
	global_load_dword v36, v[8:9], off offset:528
	global_load_dword v37, v[8:9], off offset:784
	global_load_dword v38, v[8:9], off offset:1040
	global_load_dword v39, v[8:9], off offset:1296
	global_load_dword v40, v[8:9], off offset:1552
	global_load_dword v41, v[8:9], off offset:1808
	global_load_dword v42, v[6:7], off offset:128
	global_load_dword v43, v[6:7], off offset:384
	global_load_dword v44, v[6:7], off offset:640
	global_load_dword v45, v[6:7], off offset:896
	global_load_dword v46, v[6:7], off offset:1152
	global_load_dword v47, v[6:7], off offset:1408
	global_load_dword v48, v[6:7], off offset:1664
	global_load_dword v49, v[6:7], off offset:1920
	global_load_dword v50, v[8:9], off offset:128
	global_load_dword v51, v[8:9], off offset:384
	global_load_dword v52, v[8:9], off offset:640
	global_load_dword v53, v[8:9], off offset:896
	global_load_dword v54, v[8:9], off offset:1152
	global_load_dword v55, v[8:9], off offset:1408
	global_load_dword v56, v[8:9], off offset:1664
	global_load_dword v57, v[8:9], off offset:1920
	global_load_dword v58, v[6:7], off offset:144
	global_load_dword v59, v[6:7], off offset:400
	global_load_dword v60, v[6:7], off offset:656
	global_load_dword v61, v[6:7], off offset:912
	global_load_dword v62, v[6:7], off offset:1168
	global_load_dword v63, v[6:7], off offset:1424
	global_load_dword v64, v[6:7], off offset:1680
	global_load_dword v65, v[6:7], off offset:1936
	global_load_dword v66, v[8:9], off offset:144
	global_load_dword v67, v[8:9], off offset:400
	global_load_dword v68, v[8:9], off offset:656
	global_load_dword v69, v[8:9], off offset:912
	global_load_dword v70, v[8:9], off offset:1168
	global_load_dword v71, v[8:9], off offset:1424
	global_load_dword v72, v[8:9], off offset:1680
	global_load_dword v73, v[8:9], off offset:1936
	s_waitcnt vmcnt(0)
	v_cvt_pk_bf16_f32 v10, v10, v11
	v_cvt_pk_bf16_f32 v11, v12, v13
	v_cvt_pk_bf16_f32 v12, v14, v15
	v_cvt_pk_bf16_f32 v13, v16, v17
	ds_write_b128 v146, v[10:13]
	v_cvt_pk_bf16_f32 v18, v18, v19
	v_cvt_pk_bf16_f32 v19, v20, v21
	v_cvt_pk_bf16_f32 v20, v22, v23
	v_cvt_pk_bf16_f32 v21, v24, v25
	ds_write_b128 v146, v[18:21] offset:1024
	v_cvt_pk_bf16_f32 v26, v26, v27
	v_cvt_pk_bf16_f32 v27, v28, v29
	v_cvt_pk_bf16_f32 v28, v30, v31
	v_cvt_pk_bf16_f32 v29, v32, v33
	ds_write_b128 v146, v[26:29] offset:2048
	v_cvt_pk_bf16_f32 v34, v34, v35
	v_cvt_pk_bf16_f32 v35, v36, v37
	v_cvt_pk_bf16_f32 v36, v38, v39
	v_cvt_pk_bf16_f32 v37, v40, v41
	ds_write_b128 v146, v[34:37] offset:3072
	v_cvt_pk_bf16_f32 v42, v42, v43
	v_cvt_pk_bf16_f32 v43, v44, v45
	v_cvt_pk_bf16_f32 v44, v46, v47
	v_cvt_pk_bf16_f32 v45, v48, v49
	ds_write_b128 v146, v[42:45] offset:4096
	v_cvt_pk_bf16_f32 v50, v50, v51
	v_cvt_pk_bf16_f32 v51, v52, v53
	v_cvt_pk_bf16_f32 v52, v54, v55
	v_cvt_pk_bf16_f32 v53, v56, v57
	ds_write_b128 v146, v[50:53] offset:5120
	v_cvt_pk_bf16_f32 v58, v58, v59
	v_cvt_pk_bf16_f32 v59, v60, v61
	v_cvt_pk_bf16_f32 v60, v62, v63
	v_cvt_pk_bf16_f32 v61, v64, v65
	ds_write_b128 v146, v[58:61] offset:6144
	v_cvt_pk_bf16_f32 v66, v66, v67
	v_cvt_pk_bf16_f32 v67, v68, v69
	v_cvt_pk_bf16_f32 v68, v70, v71
	v_cvt_pk_bf16_f32 v69, v72, v73
	ds_write_b128 v146, v[66:69] offset:7168
	s_add_u32 s14, s12, s16
	s_addc_u32 s15, s13, s17
	s_add_u32 s0, s14, 0x2000
	s_addc_u32 s1, s15, 0
	v_lshl_add_u64 v[6:7], s[14:15], 0, v[4:5]
	v_lshl_add_u64 v[8:9], s[0:1], 0, v[4:5]
	s_waitcnt lgkmcnt(0)
; #define LAS __attribute__((address_space(3)))
; #define LDS_WAIT() asm volatile("s_waitcnt lgkmcnt(0)" ::: "memory")
; __device__ __forceinline__ unsigned pk2(float lo, float hi) { const pk2_f32x2 v = {lo, hi}; return __builtin_bit_cast(unsigned, __builtin_convertvector(v, pk2_bf16x2)); }
; #define REC_LOAD_TILE(dst_, tile_) do { const int t_ = t0 + (tile_) * 16 + fr; _Pragma("unroll") for (int kk_ = 0; kk_ < 2; ++kk_) _Pragma("unroll") for (int j_ = 0; j_ < 4; ++j_) { const int tt_ = t_ - 3 + j_; \
;         dst_[kk_][j_] = *(const u32x4*)(zb + (size_t)(tt_ > 0 ? tt_ : 0) * ZP + 32 * kk_ + 8 * q); } } while (0)
; __device__ __forceinline__ void rec1_unit(KArgs args, int L, int unit, LAS unsigned char* lds, int wave, int lane) {
;     ...
;     for (int f = 0; f < 16; ++f) { const int mat = f >> 3, n = (f >> 1) & 3, kk = f & 1; const float* W = mat ? Wx : Wa;
;         const int jout = 8 * (fr >> 2) + (fr & 3) + 4 * (n & 1) + 32 * (n >> 1); const float* wp = W + (32 * kk + 8 * q) * 64 + jout;
;         u32x4 w; w.x = pk2(wp[0], wp[64]); w.y = pk2(wp[128], wp[192]); w.z = pk2(wp[256], wp[320]); w.w = pk2(wp[384], wp[448]);
;         *(LAS u32x4*)(wl + f * 1024 + lane * 16) = w; }
;     LAS float* ct = (LAS float*)(lds + 131072 + wave * 2048);
;     { const int c = 64 * hb + lane; const float* cw = args->in[I_CONVW] + (size_t)L * 4 * 512;
;       ct[lane * 8 + 0] = cw[c]; ct[lane * 8 + 1] = cw[512 + c]; ct[lane * 8 + 2] = cw[1024 + c]; ct[lane * 8 + 3] = cw[1536 + c];
;       ct[lane * 8 + 4] = args->in[I_CONVB][L * 512 + c]; ct[lane * 8 + 5] = args->in[I_BA][L * 512 + c]; ct[lane * 8 + 6] = args->in[I_BX][L * 512 + c];
;       ct[lane * 8 + 7] = ((const float*)(ws + WS_C8))[L * 512 + c]; }
;     LDS_WAIT();
;     float Acar[2][8], Hcar[2][8];
; #pragma unroll
;     for (int kk = 0; kk < 2; ++kk)
; #pragma unroll
;         for (int e = 0; e < 8; ++e) { Acar[kk][e] = 1.f; Hcar[kk][e] = 0.f; }
;     const bf16* zb = z + (size_t)(b * SEQ) * ZP + ZC_XR + 64 * hb;
;     const int bidx15 = ((lane & ~15) | 15) << 2;
;     u32x4 rawc[2][4];
;     ...
;     REC_LOAD_TILE(rawc, 0);
	global_load_dword v10, v[6:7], off
	global_load_dword v11, v[6:7], off offset:256
	global_load_dword v12, v[6:7], off offset:512
	global_load_dword v13, v[6:7], off offset:768
	global_load_dword v14, v[6:7], off offset:1024
	global_load_dword v15, v[6:7], off offset:1280
	global_load_dword v16, v[6:7], off offset:1536
	global_load_dword v17, v[6:7], off offset:1792
	global_load_dword v18, v[8:9], off
	global_load_dword v19, v[8:9], off offset:256
	global_load_dword v20, v[8:9], off offset:512
	global_load_dword v21, v[8:9], off offset:768
	global_load_dword v22, v[8:9], off offset:1024
	global_load_dword v23, v[8:9], off offset:1280
	global_load_dword v24, v[8:9], off offset:1536
	global_load_dword v25, v[8:9], off offset:1792
	global_load_dword v26, v[6:7], off offset:16
	global_load_dword v27, v[6:7], off offset:272
	global_load_dword v28, v[6:7], off offset:528
	global_load_dword v29, v[6:7], off offset:784
	global_load_dword v30, v[6:7], off offset:1040
	global_load_dword v31, v[6:7], off offset:1296
	global_load_dword v32, v[6:7], off offset:1552
	global_load_dword v33, v[6:7], off offset:1808
	global_load_dword v34, v[8:9], off offset:16
	global_load_dword v35, v[8:9], off offset:272
	global_load_dword v36, v[8:9], off offset:528
	global_load_dword v37, v[8:9], off offset:784
	global_load_dword v38, v[8:9], off offset:1040
	global_load_dword v39, v[8:9], off offset:1296
	global_load_dword v40, v[8:9], off offset:1552
	global_load_dword v41, v[8:9], off offset:1808
	global_load_dword v42, v[6:7], off offset:128
	global_load_dword v43, v[6:7], off offset:384
	global_load_dword v44, v[6:7], off offset:640
	global_load_dword v45, v[6:7], off offset:896
	global_load_dword v46, v[6:7], off offset:1152
	global_load_dword v47, v[6:7], off offset:1408
	global_load_dword v48, v[6:7], off offset:1664
	global_load_dword v49, v[6:7], off offset:1920
	global_load_dword v50, v[8:9], off offset:128
	global_load_dword v51, v[8:9], off offset:384
	global_load_dword v52, v[8:9], off offset:640
	global_load_dword v53, v[8:9], off offset:896
	global_load_dword v54, v[8:9], off offset:1152
	global_load_dword v55, v[8:9], off offset:1408
	global_load_dword v56, v[8:9], off offset:1664
	global_load_dword v57, v[8:9], off offset:1920
	global_load_dword v58, v[6:7], off offset:144
	global_load_dword v59, v[6:7], off offset:400
	global_load_dword v60, v[6:7], off offset:656
	global_load_dword v61, v[6:7], off offset:912
	global_load_dword v62, v[6:7], off offset:1168
	global_load_dword v63, v[6:7], off offset:1424
	global_load_dword v64, v[6:7], off offset:1680
	global_load_dword v65, v[6:7], off offset:1936
	global_load_dword v66, v[8:9], off offset:144
	global_load_dword v67, v[8:9], off offset:400
	global_load_dword v68, v[8:9], off offset:656
	global_load_dword v69, v[8:9], off offset:912
	global_load_dword v70, v[8:9], off offset:1168
	global_load_dword v71, v[8:9], off offset:1424
	global_load_dword v72, v[8:9], off offset:1680
	global_load_dword v73, v[8:9], off offset:1936
	s_waitcnt vmcnt(0)
	v_cvt_pk_bf16_f32 v10, v10, v11
	v_cvt_pk_bf16_f32 v11, v12, v13
	v_cvt_pk_bf16_f32 v12, v14, v15
	v_cvt_pk_bf16_f32 v13, v16, v17
	ds_write_b128 v146, v[10:13] offset:8192
	v_cvt_pk_bf16_f32 v18, v18, v19
	v_cvt_pk_bf16_f32 v19, v20, v21
	v_cvt_pk_bf16_f32 v20, v22, v23
	v_cvt_pk_bf16_f32 v21, v24, v25
	ds_write_b128 v146, v[18:21] offset:9216
	v_cvt_pk_bf16_f32 v26, v26, v27
	v_cvt_pk_bf16_f32 v27, v28, v29
	v_cvt_pk_bf16_f32 v28, v30, v31
	v_cvt_pk_bf16_f32 v29, v32, v33
	ds_write_b128 v146, v[26:29] offset:10240
	v_cvt_pk_bf16_f32 v34, v34, v35
	v_cvt_pk_bf16_f32 v35, v36, v37
	v_cvt_pk_bf16_f32 v36, v38, v39
	v_cvt_pk_bf16_f32 v37, v40, v41
	ds_write_b128 v146, v[34:37] offset:11264
	v_cvt_pk_bf16_f32 v42, v42, v43
	v_cvt_pk_bf16_f32 v43, v44, v45
	v_cvt_pk_bf16_f32 v44, v46, v47
	v_cvt_pk_bf16_f32 v45, v48, v49
	ds_write_b128 v146, v[42:45] offset:12288
	v_cvt_pk_bf16_f32 v50, v50, v51
	v_cvt_pk_bf16_f32 v51, v52, v53
	v_cvt_pk_bf16_f32 v52, v54, v55
	v_cvt_pk_bf16_f32 v53, v56, v57
	ds_write_b128 v146, v[50:53] offset:13312
	v_cvt_pk_bf16_f32 v58, v58, v59
	v_cvt_pk_bf16_f32 v59, v60, v61
	v_cvt_pk_bf16_f32 v60, v62, v63
	v_cvt_pk_bf16_f32 v61, v64, v65
	ds_write_b128 v146, v[58:61] offset:14336
	v_cvt_pk_bf16_f32 v66, v66, v67
	v_cvt_pk_bf16_f32 v67, v68, v69
	v_cvt_pk_bf16_f32 v68, v70, v71
	v_cvt_pk_bf16_f32 v69, v72, v73
	ds_write_b128 v146, v[66:69] offset:15360
	global_load_dword v4, v[100:101], off
	global_load_dword v5, v[100:101], off offset:2048
	global_load_dword v6, v[102:103], off
	global_load_dword v7, v[104:105], off
	global_load_dword v8, v[106:107], off
	global_load_dword v9, v[108:109], off
	global_load_dword v10, v[110:111], off
	global_load_dword v11, v[112:113], off
	s_lshl_b32 s0, s10, 8
	s_and_b32 s4, s0, 0xf00
	s_and_b32 s0, s0, 0xfffff000
	v_add_u32_e32 v152, s4, v148
	v_mad_i64_i32 v[2:3], s[0:1], s0, v209, v[114:115]
	v_or_b32_e32 v12, s4, v147
	v_max_i32_e32 v14, 0, v152
	v_max_i32_e32 v16, -1, v152
	v_max_i32_e32 v17, -2, v152
	v_mov_b32_e32 v13, v0
	v_mul_u32_u24_e32 v12, 0x1400, v12
	v_mad_u64_u32 v[14:15], s[0:1], v14, s88, v[2:3]
	v_add_u32_e32 v16, 1, v16
	v_add_u32_e32 v18, 2, v17
	v_lshl_add_u64 v[12:13], v[2:3], 0, v[12:13]
	v_mad_u64_u32 v[16:17], s[0:1], v16, s88, v[2:3]
	v_mad_u64_u32 v[18:19], s[0:1], v18, s88, v[2:3]
	s_and_b32 s11, s27, 0xf00
	s_and_b32 s0, s27, 0xfffff000
	v_or_b32_e32 v153, s11, v147
	s_waitcnt lgkmcnt(3)
	v_mov_b32_e32 v116, 0
	v_or_b32_e32 v154, s0, v153
	s_mov_b32 s29, 16
	v_mov_b32_e32 v117, v116
	v_mov_b32_e32 v118, v116
	v_mov_b32_e32 v119, v116
	v_mov_b32_e32 v120, v116
	v_mov_b32_e32 v121, v116
	v_mov_b32_e32 v122, v116
	v_mov_b32_e32 v123, v116
	v_mov_b32_e32 v128, v116
	v_mov_b32_e32 v129, v116
	v_mov_b32_e32 v134, v116
	v_mov_b32_e32 v135, v116
	v_mov_b32_e32 v138, v116
	v_mov_b32_e32 v139, v116
	s_waitcnt vmcnt(4)
	ds_write_b128 v151, v[4:7]
	s_waitcnt vmcnt(0)
	v_mul_f32_e32 v9, 0xbfb8aa3b, v9
	v_mul_f32_e32 v10, 0xbfb8aa3b, v10
	ds_write_b128 v151, v[8:11] offset:16
	s_waitcnt lgkmcnt(0)
	global_load_dwordx4 v[74:77], v[14:15], off
	global_load_dwordx4 v[58:61], v[14:15], off offset:64
	global_load_dwordx4 v[70:73], v[16:17], off
	global_load_dwordx4 v[54:57], v[16:17], off offset:64
	global_load_dwordx4 v[66:69], v[18:19], off
	global_load_dwordx4 v[50:53], v[18:19], off offset:64
	global_load_dwordx4 v[62:65], v[12:13], off
	global_load_dwordx4 v[46:49], v[12:13], off offset:64
	v_mov_b32_e32 v4, 1.0
	v_mov_b32_e32 v5, v4
	v_mov_b32_e32 v8, v4
	v_mov_b32_e32 v9, v4
	v_mov_b32_e32 v12, v4
	v_mov_b32_e32 v13, v4
	v_mov_b32_e32 v6, v116
	v_mov_b32_e32 v7, v116
	v_mov_b32_e32 v136, v4
	v_mov_b32_e32 v137, v4
	v_mov_b32_e32 v132, v4
	v_mov_b32_e32 v133, v4
	v_mov_b32_e32 v130, v4
	v_mov_b32_e32 v131, v4
	v_mov_b32_e32 v126, v4
	v_mov_b32_e32 v127, v4
	s_waitcnt lgkmcnt(4)
	v_mov_b32_e32 v124, v4
	s_waitcnt lgkmcnt(3)
	v_mov_b32_e32 v125, v4
; __device__ __forceinline__ unsigned pk2(float lo, float hi) { const pk2_f32x2 v = {lo, hi}; return __builtin_bit_cast(unsigned, __builtin_convertvector(v, pk2_bf16x2)); }
; #define REC_LOAD_TILE(dst_, tile_) do { const int t_ = t0 + (tile_) * 16 + fr; _Pragma("unroll") for (int kk_ = 0; kk_ < 2; ++kk_) _Pragma("unroll") for (int j_ = 0; j_ < 4; ++j_) { const int tt_ = t_ - 3 + j_; \
;         dst_[kk_][j_] = *(const u32x4*)(zb + (size_t)(tt_ > 0 ? tt_ : 0) * ZP + 32 * kk_ + 8 * q); } } while (0)
; __device__ __forceinline__ void rec1_unit(KArgs args, int L, int unit, LAS unsigned char* lds, int wave, int lane) {
;     ...
;     REC_LOAD_TILE(rawc, 0);
; #pragma unroll 1
;     for (int tile = 0; tile < 16; ++tile) {
;         const int t = t0 + tile * 16 + fr; const bool edge = (t0 + tile * 16) == 0;
;         u32x4 rawn[2][4];
;         REC_LOAD_TILE(rawn, tile < 15 ? tile + 1 : 15);
;         u32x4 xb[2];
; #pragma unroll
;         for (int kk = 0; kk < 2; ++kk) {
;             float xc[8];
; #pragma unroll
;             for (int e = 0; e < 8; ++e) xc[e] = ct[(32 * kk + 8 * q + e) * 8 + 4];
; #pragma unroll
;             for (int j = 0; j < 4; ++j) { const int tt = t - 3 + j;
;                 u32x4 raw = rawc[kk][j];
;                 if (edge && tt < 0) raw = (u32x4){0u, 0u, 0u, 0u};
;                 const float xv[8] = {bflo(raw.x), bfhi(raw.x), bflo(raw.y), bfhi(raw.y), bflo(raw.z), bfhi(raw.z), bflo(raw.w), bfhi(raw.w)};
; #pragma unroll
;                 for (int e = 0; e < 8; ++e) xc[e] += ct[(32 * kk + 8 * q + e) * 8 + j] * xv[e]; }
;             xb[kk].x = pk2(xc[0], xc[1]); xb[kk].y = pk2(xc[2], xc[3]); xb[kk].z = pk2(xc[4], xc[5]); xb[kk].w = pk2(xc[6], xc[7]);
.LBB0_178:
	s_add_i32 s4, s11, s29
	s_cmpk_lg_i32 s29, 0x100
	s_cselect_b32 s0, s29, 0xf0
	v_add_u32_e32 v26, s0, v152
	v_add_u32_e32 v155, s29, v153
	v_max_i32_e32 v10, 0, v26
	v_max_i32_e32 v18, -1, v26
	v_max_i32_e32 v22, -2, v26
	v_max_i32_e32 v26, -3, v26
	v_add_u32_e32 v164, -16, v155
	v_add_u32_e32 v18, 1, v18
	v_add_u32_e32 v22, 2, v22
	v_add_u32_e32 v26, 3, v26
	s_cmp_eq_u32 s4, 16
	v_mad_u64_u32 v[10:11], s[0:1], v10, s88, v[2:3]
	v_mad_u64_u32 v[34:35], s[0:1], v18, s88, v[2:3]
	v_mad_u64_u32 v[38:39], s[0:1], v22, s88, v[2:3]
	v_mad_u64_u32 v[42:43], s[0:1], v26, s88, v[2:3]
	s_cselect_b64 s[20:21], -1, 0
	v_cmp_gt_u32_e64 s[4:5], 3, v164
	s_and_b64 s[0:1], s[20:21], s[4:5]
	v_cmp_gt_u32_e64 s[4:5], 2, v164
	global_load_dwordx4 v[14:17], v[10:11], off
	global_load_dwordx4 v[18:21], v[34:35], off
	global_load_dwordx4 v[22:25], v[38:39], off
	global_load_dwordx4 v[26:29], v[42:43], off
	global_load_dwordx4 v[30:33], v[10:11], off offset:64
	s_nop 0
	global_load_dwordx4 v[34:37], v[34:35], off offset:64
	s_nop 0
	global_load_dwordx4 v[38:41], v[38:39], off offset:64
	s_nop 0
	global_load_dwordx4 v[42:45], v[42:43], off offset:64
	ds_read_b128 v[78:81], v150
	ds_read2_b32 v[160:161], v150 offset0:4 offset1:12
	ds_read_b128 v[156:159], v150 offset:32
	ds_read2_b32 v[162:163], v150 offset0:20 offset1:28
	ds_read2_b32 v[140:141], v150 offset0:36 offset1:44
	ds_read2_b32 v[10:11], v150 offset0:52 offset1:60
	s_and_b64 s[14:15], s[20:21], s[4:5]
	v_cmp_eq_u32_e64 s[4:5], 16, v155
	s_waitcnt vmcnt(15)
	v_cndmask_b32_e64 v74, v74, 0, s[0:1]
	s_and_b64 s[4:5], s[20:21], s[4:5]
	s_waitcnt vmcnt(13)
	v_cndmask_b32_e64 v168, v71, 0, s[14:15]
	v_cndmask_b32_e64 v70, v70, 0, s[14:15]
	s_waitcnt vmcnt(11)
	v_cndmask_b32_e64 v155, v69, 0, s[4:5]
	v_cndmask_b32_e64 v169, v68, 0, s[4:5]
	v_cndmask_b32_e64 v170, v67, 0, s[4:5]
	v_cndmask_b32_e64 v71, v66, 0, s[4:5]
	v_lshlrev_b32_e32 v66, 16, v74
	v_and_b32_e32 v67, 0xffff0000, v74
	s_waitcnt lgkmcnt(5)
	v_mov_b32_e32 v68, v78
	s_waitcnt lgkmcnt(3)
	v_mov_b32_e32 v69, v156
	v_pk_fma_f32 v[66:67], v[68:69], v[66:67], v[160:161]
	v_lshlrev_b32_e32 v68, 16, v70
	v_and_b32_e32 v69, 0xffff0000, v70
	v_mov_b32_e32 v156, v79
	v_pk_fma_f32 v[66:67], v[156:157], v[68:69], v[66:67]
	v_lshlrev_b32_e32 v68, 16, v71
	v_and_b32_e32 v69, 0xffff0000, v71
	v_mov_b32_e32 v70, v80
	v_mov_b32_e32 v71, v158
	v_cndmask_b32_e64 v75, v75, 0, s[0:1]
	v_pk_fma_f32 v[66:67], v[70:71], v[68:69], v[66:67]
	s_waitcnt vmcnt(9)
	v_lshlrev_b32_e32 v68, 16, v62
	v_and_b32_e32 v69, 0xffff0000, v62
	v_mov_b32_e32 v158, v81
	v_cndmask_b32_e64 v165, v77, 0, s[0:1]
	v_cndmask_b32_e64 v166, v76, 0, s[0:1]
	v_cndmask_b32_e64 v164, v73, 0, s[14:15]
	v_cndmask_b32_e64 v167, v72, 0, s[14:15]
	v_pk_fma_f32 v[66:67], v[158:159], v[68:69], v[66:67]
	v_lshlrev_b32_e32 v76, 16, v75
	v_and_b32_e32 v77, 0xffff0000, v75
	ds_read_b128 v[68:71], v150 offset:64
	ds_read_b128 v[72:75], v150 offset:96
	v_lshlrev_b32_e32 v62, 16, v63
	v_and_b32_e32 v63, 0xffff0000, v63
	v_cvt_pk_bf16_f32 v66, v66, v67
	s_waitcnt lgkmcnt(1)
	v_mov_b32_e32 v78, v68
	s_waitcnt lgkmcnt(0)
	v_mov_b32_e32 v79, v72
	v_pk_fma_f32 v[76:77], v[78:79], v[76:77], v[162:163]
	v_lshlrev_b32_e32 v78, 16, v168
	v_and_b32_e32 v79, 0xffff0000, v168
	v_mov_b32_e32 v72, v69
	v_pk_fma_f32 v[68:69], v[72:73], v[78:79], v[76:77]
	v_lshlrev_b32_e32 v72, 16, v170
	v_and_b32_e32 v73, 0xffff0000, v170
	v_mov_b32_e32 v76, v70
	v_mov_b32_e32 v77, v74
	v_pk_fma_f32 v[68:69], v[76:77], v[72:73], v[68:69]
	v_mov_b32_e32 v74, v71
	v_pk_fma_f32 v[62:63], v[74:75], v[62:63], v[68:69]
	ds_read_b128 v[68:71], v150 offset:128
	ds_read_b128 v[72:75], v150 offset:160
	v_lshlrev_b32_e32 v76, 16, v166
	v_and_b32_e32 v77, 0xffff0000, v166
	v_cvt_pk_bf16_f32 v67, v62, v63
	s_waitcnt lgkmcnt(1)
	v_mov_b32_e32 v78, v68
	s_waitcnt lgkmcnt(0)
	v_mov_b32_e32 v79, v72
	v_pk_fma_f32 v[76:77], v[78:79], v[76:77], v[140:141]
	v_lshlrev_b32_e32 v78, 16, v167
	v_and_b32_e32 v79, 0xffff0000, v167
	v_mov_b32_e32 v72, v69
	v_pk_fma_f32 v[68:69], v[72:73], v[78:79], v[76:77]
	v_lshlrev_b32_e32 v72, 16, v169
	v_and_b32_e32 v73, 0xffff0000, v169
	v_mov_b32_e32 v76, v70
	v_mov_b32_e32 v77, v74
	v_pk_fma_f32 v[68:69], v[76:77], v[72:73], v[68:69]
	v_lshlrev_b32_e32 v72, 16, v64
	v_and_b32_e32 v73, 0xffff0000, v64
	v_mov_b32_e32 v74, v71
	v_pk_fma_f32 v[76:77], v[74:75], v[72:73], v[68:69]
	ds_read_b128 v[68:71], v150 offset:192
	ds_read_b128 v[72:75], v150 offset:224
	v_lshlrev_b32_e32 v78, 16, v165
	v_and_b32_e32 v79, 0xffff0000, v165
	v_lshlrev_b32_e32 v64, 16, v65
	s_waitcnt lgkmcnt(1)
	v_mov_b32_e32 v80, v68
	s_waitcnt lgkmcnt(0)
	v_mov_b32_e32 v81, v72
	v_pk_fma_f32 v[10:11], v[80:81], v[78:79], v[10:11]
	v_lshlrev_b32_e32 v78, 16, v164
	v_and_b32_e32 v79, 0xffff0000, v164
	v_mov_b32_e32 v72, v69
	v_pk_fma_f32 v[10:11], v[72:73], v[78:79], v[10:11]
	v_lshlrev_b32_e32 v68, 16, v155
	v_and_b32_e32 v69, 0xffff0000, v155
	v_mov_b32_e32 v72, v70
	v_mov_b32_e32 v73, v74
	v_pk_fma_f32 v[10:11], v[72:73], v[68:69], v[10:11]
	v_and_b32_e32 v65, 0xffff0000, v65
	v_mov_b32_e32 v74, v71
	v_pk_fma_f32 v[10:11], v[74:75], v[64:65], v[10:11]
	v_cvt_pk_bf16_f32 v68, v76, v77
	v_cvt_pk_bf16_f32 v69, v10, v11
	v_add_u32_e32 v10, 0x400, v150
	ds_read2_b32 v[64:65], v10 offset0:4 offset1:12
	ds_read2_b32 v[70:71], v10 offset0:20 offset1:28
	ds_read2_b32 v[62:63], v10 offset0:36 offset1:44
	ds_read2_b32 v[10:11], v10 offset0:52 offset1:60
	v_cndmask_b32_e64 v75, v57, 0, s[14:15]
	v_cndmask_b32_e64 v76, v56, 0, s[14:15]
	v_cndmask_b32_e64 v77, v55, 0, s[14:15]
	v_cndmask_b32_e64 v78, v54, 0, s[14:15]
	v_cndmask_b32_e64 v79, v53, 0, s[4:5]
	v_cndmask_b32_e64 v80, v52, 0, s[4:5]
	v_cndmask_b32_e64 v81, v51, 0, s[4:5]
	v_cndmask_b32_e64 v140, v50, 0, s[4:5]
	ds_read_b128 v[50:53], v150 offset:1024
	ds_read_b128 v[54:57], v150 offset:1056
	v_cndmask_b32_e64 v74, v59, 0, s[0:1]
	v_cndmask_b32_e64 v59, v58, 0, s[0:1]
	v_cndmask_b32_e64 v72, v61, 0, s[0:1]
	v_cndmask_b32_e64 v73, v60, 0, s[0:1]
	v_lshlrev_b32_e32 v58, 16, v59
	v_and_b32_e32 v59, 0xffff0000, v59
	s_waitcnt lgkmcnt(1)
; #define LAS __attribute__((address_space(3)))
; __device__ __forceinline__ float fsigmoid(float x) { return __builtin_amdgcn_rcpf(1.f + __builtin_amdgcn_exp2f(-x * LOG2E)); }
; #define REC_SCAN_STEP(N_) asm volatile("s_nop 1\n\tv_fmac_f32_dpp %0, %0, %1 row_shr:" #N_ " row_mask:0xf bank_mask:0xf\n\ts_nop 1\n\tv_mul_f32_dpp %1, %1, %1 row_shr:" #N_ " row_mask:0xf bank_mask:0xf" : "+v"(bb), "+v"(a))
; __device__ __forceinline__ void rec1_unit(KArgs args, int L, int unit, LAS unsigned char* lds, int wave, int lane) {
;     ...
;         asm volatile("" ::: "memory");
; #pragma unroll
;         for (int kh = 0; kh < 2; ++kh) {
;             f32x4 racc[2], iacc[2];
; #pragma unroll
;             for (int nn = 0; nn < 2; ++nn) { racc[nn] = (f32x4){0.f, 0.f, 0.f, 0.f}; iacc[nn] = (f32x4){0.f, 0.f, 0.f, 0.f};
; #pragma unroll
;                 for (int kk = 0; kk < 2; ++kk) { const int n = 2 * kh + nn;
;                     const bf16x8 fa = *(const LAS bf16x8*)(wl + ((0 * 4 + n) * 2 + kk) * 1024 + lane * 16), fx = *(const LAS bf16x8*)(wl + ((1 * 4 + n) * 2 + kk) * 1024 + lane * 16);
;                     const bf16x8 xk = __builtin_bit_cast(bf16x8, xb[kk]);
;                     racc[nn] = __builtin_amdgcn_mfma_f32_16x16x32_bf16(fa, xk, racc[nn], 0, 0, 0); iacc[nn] = __builtin_amdgcn_mfma_f32_16x16x32_bf16(fx, xk, iacc[nn], 0, 0, 0); } }
;             const unsigned xw[4] = {xb[kh].x, xb[kh].y, xb[kh].z, xb[kh].w};
;             float hv[8], av[8];
; #pragma unroll
;             for (int e = 0; e < 8; ++e) {
;                 const int nn = e >> 2, jj = e & 3; const int cb = (32 * kh + 8 * q + e) * 8;
;                 const float xcv = (e & 1) ? bfhi(xw[e >> 1]) : bflo(xw[e >> 1]);
;                 const float r = fsigmoid(racc[nn][jj] + ct[cb + 5]), ig = fsigmoid(iacc[nn][jj] + ct[cb + 6]);
;                 float a = __builtin_amdgcn_exp2f(ct[cb + 7] * r);
;                 float bb = __builtin_amdgcn_sqrtf(fmaxf(1.f - a * a, 0.f)) * (ig * xcv);
;     ...
;                 REC_SCAN_STEP(1); REC_SCAN_STEP(2); REC_SCAN_STEP(4); REC_SCAN_STEP(8);
	v_mov_b32_e32 v60, v50
	s_waitcnt lgkmcnt(0)
	v_mov_b32_e32 v61, v54
	v_pk_fma_f32 v[58:59], v[60:61], v[58:59], v[64:65]
	v_lshlrev_b32_e32 v60, 16, v78
	v_and_b32_e32 v61, 0xffff0000, v78
	v_mov_b32_e32 v54, v51
	v_pk_fma_f32 v[50:51], v[54:55], v[60:61], v[58:59]
	v_lshlrev_b32_e32 v54, 16, v140
	v_and_b32_e32 v55, 0xffff0000, v140
	v_mov_b32_e32 v58, v52
	v_mov_b32_e32 v59, v56
	v_pk_fma_f32 v[50:51], v[58:59], v[54:55], v[50:51]
	s_waitcnt vmcnt(8)
	v_lshlrev_b32_e32 v54, 16, v46
	v_and_b32_e32 v55, 0xffff0000, v46
	v_mov_b32_e32 v56, v53
	v_pk_fma_f32 v[50:51], v[56:57], v[54:55], v[50:51]
	ds_read_b128 v[52:55], v150 offset:1088
	ds_read_b128 v[56:59], v150 offset:1120
	v_lshlrev_b32_e32 v60, 16, v74
	v_and_b32_e32 v61, 0xffff0000, v74
	v_lshlrev_b32_e32 v46, 16, v47
	s_waitcnt lgkmcnt(1)
	v_mov_b32_e32 v64, v52
	s_waitcnt lgkmcnt(0)
	v_mov_b32_e32 v65, v56
	v_pk_fma_f32 v[60:61], v[64:65], v[60:61], v[70:71]
	v_lshlrev_b32_e32 v64, 16, v77
	v_and_b32_e32 v65, 0xffff0000, v77
	v_mov_b32_e32 v56, v53
	v_pk_fma_f32 v[52:53], v[56:57], v[64:65], v[60:61]
	v_lshlrev_b32_e32 v56, 16, v81
	v_and_b32_e32 v57, 0xffff0000, v81
	v_mov_b32_e32 v60, v54
	v_mov_b32_e32 v61, v58
	v_pk_fma_f32 v[52:53], v[60:61], v[56:57], v[52:53]
	v_and_b32_e32 v47, 0xffff0000, v47
	v_mov_b32_e32 v58, v55
	v_pk_fma_f32 v[60:61], v[58:59], v[46:47], v[52:53]
	ds_read_b128 v[52:55], v150 offset:1152
	ds_read_b128 v[56:59], v150 offset:1184
	v_lshlrev_b32_e32 v46, 16, v73
	v_and_b32_e32 v47, 0xffff0000, v73
	s_waitcnt lgkmcnt(1)
	v_mov_b32_e32 v64, v52
	s_waitcnt lgkmcnt(0)
	v_mov_b32_e32 v65, v56
	v_pk_fma_f32 v[46:47], v[64:65], v[46:47], v[62:63]
	v_lshlrev_b32_e32 v62, 16, v76
	v_and_b32_e32 v63, 0xffff0000, v76
	v_mov_b32_e32 v56, v53
	v_pk_fma_f32 v[46:47], v[56:57], v[62:63], v[46:47]
	v_lshlrev_b32_e32 v52, 16, v80
	v_and_b32_e32 v53, 0xffff0000, v80
	v_mov_b32_e32 v56, v54
	v_mov_b32_e32 v57, v58
	v_pk_fma_f32 v[46:47], v[56:57], v[52:53], v[46:47]
	v_lshlrev_b32_e32 v52, 16, v48
	v_and_b32_e32 v53, 0xffff0000, v48
	v_mov_b32_e32 v58, v55
	v_pk_fma_f32 v[62:63], v[58:59], v[52:53], v[46:47]
	ds_read_b128 v[52:55], v150 offset:1216
	ds_read_b128 v[56:59], v150 offset:1248
	v_lshlrev_b32_e32 v46, 16, v72
	v_and_b32_e32 v47, 0xffff0000, v72
	s_waitcnt lgkmcnt(1)
	v_mov_b32_e32 v64, v52
	s_waitcnt lgkmcnt(0)
	v_mov_b32_e32 v65, v56
	v_pk_fma_f32 v[10:11], v[64:65], v[46:47], v[10:11]
	v_lshlrev_b32_e32 v46, 16, v75
	v_and_b32_e32 v47, 0xffff0000, v75
	v_mov_b32_e32 v56, v53
	v_pk_fma_f32 v[10:11], v[56:57], v[46:47], v[10:11]
	v_lshlrev_b32_e32 v46, 16, v79
	v_and_b32_e32 v47, 0xffff0000, v79
	v_mov_b32_e32 v52, v54
	v_mov_b32_e32 v53, v58
	v_pk_fma_f32 v[10:11], v[52:53], v[46:47], v[10:11]
	v_lshlrev_b32_e32 v46, 16, v49
	v_and_b32_e32 v47, 0xffff0000, v49
	v_mov_b32_e32 v58, v55
	v_pk_fma_f32 v[10:11], v[58:59], v[46:47], v[10:11]
	v_cvt_pk_bf16_f32 v46, v50, v51
	ds_read_b128 v[50:53], v146
	ds_read_b128 v[54:57], v146 offset:8192
	v_cvt_pk_bf16_f32 v47, v60, v61
	v_cvt_pk_bf16_f32 v48, v62, v63
	ds_read_b128 v[58:61], v146 offset:1024
	ds_read_b128 v[62:65], v146 offset:9216
	s_waitcnt lgkmcnt(3)
	v_mfma_f32_16x16x32_bf16 v[50:53], v[50:53], v[66:69], 0
	v_cvt_pk_bf16_f32 v49, v10, v11
	v_add3_u32 v10, v154, s29, -16
	v_ashrrev_i32_e32 v11, 31, v10
	s_waitcnt lgkmcnt(2)
	v_mfma_f32_16x16x32_bf16 v[54:57], v[54:57], v[66:69], 0
	v_lshlrev_b64 v[10:11], 9, v[10:11]
	v_lshl_add_u64 v[10:11], v[10:11], 0, v[82:83]
	v_lshlrev_b64 v[10:11], 1, v[10:11]
	s_waitcnt lgkmcnt(1)
	v_mfma_f32_16x16x32_bf16 v[50:53], v[58:61], v[46:49], v[50:53]
	s_add_i32 s29, s29, 16
	s_cmpk_eq_i32 s29, 0x110
	s_waitcnt lgkmcnt(0)
	v_mfma_f32_16x16x32_bf16 v[54:57], v[62:65], v[46:49], v[54:57]
	ds_read_b128 v[58:61], v146 offset:2048
	ds_read_b128 v[62:65], v146 offset:10240
	ds_read_b128 v[70:73], v146 offset:3072
	ds_read_b128 v[74:77], v146 offset:11264
	s_waitcnt lgkmcnt(3)
	v_mfma_f32_16x16x32_bf16 v[58:61], v[58:61], v[66:69], 0
	s_waitcnt lgkmcnt(1)
	v_mfma_f32_16x16x32_bf16 v[58:61], v[70:73], v[46:49], v[58:61]
	ds_read2_b32 v[70:71], v150 offset0:5 offset1:6
	v_lshlrev_b32_e32 v72, 16, v66
	s_waitcnt lgkmcnt(0)
	v_fmamk_f32 v50, v50, 0xbfb8aa3b, v70
	s_nop 0
	v_exp_f32_e32 v50, v50
	ds_read_b32 v70, v150 offset:28
	v_fmamk_f32 v54, v54, 0xbfb8aa3b, v71
	s_nop 0
	v_add_f32_e32 v50, 1.0, v50
	v_rcp_f32_e32 v50, v50
	v_exp_f32_e32 v54, v54
	v_mfma_f32_16x16x32_bf16 v[62:65], v[62:65], v[66:69], 0
	s_waitcnt lgkmcnt(0)
	v_mul_f32_e32 v50, v70, v50
	v_exp_f32_e32 v71, v50
	v_add_f32_e32 v54, 1.0, v54
	v_rcp_f32_e32 v54, v54
	v_mfma_f32_16x16x32_bf16 v[62:65], v[74:77], v[46:49], v[62:65]
	v_fma_f32 v50, -v71, v71, 1.0
	v_max_f32_e32 v50, 0, v50
	v_sqrt_f32_e32 v50, v50
	v_mul_f32_e32 v54, v54, v72
	v_mul_f32_e32 v73, v54, v50
	s_nop 1
	v_fmac_f32_dpp v73, v73, v71 row_shr:1 row_mask:0xf bank_mask:0xf
	s_nop 1
	v_mul_f32_dpp v71, v71, v71 row_shr:1 row_mask:0xf bank_mask:0xf
	v_and_b32_e32 v50, 0xffff0000, v66
	s_nop 1
	v_fmac_f32_dpp v73, v73, v71 row_shr:2 row_mask:0xf bank_mask:0xf
	s_nop 1
	v_mul_f32_dpp v71, v71, v71 row_shr:2 row_mask:0xf bank_mask:0xf
	s_nop 0
	s_nop 1
	v_fmac_f32_dpp v73, v73, v71 row_shr:4 row_mask:0xf bank_mask:0xf
	s_nop 1
	v_mul_f32_dpp v71, v71, v71 row_shr:4 row_mask:0xf bank_mask:0xf
	s_nop 0
	s_nop 1
	v_fmac_f32_dpp v73, v73, v71 row_shr:8 row_mask:0xf bank_mask:0xf
	s_nop 1
	v_mul_f32_dpp v71, v71, v71 row_shr:8 row_mask:0xf bank_mask:0xf
	ds_read2_b32 v[74:75], v150 offset0:13 offset1:14
	s_waitcnt lgkmcnt(0)
	v_fmamk_f32 v51, v51, 0xbfb8aa3b, v74
	s_nop 0
	v_exp_f32_e32 v51, v51
	v_fmamk_f32 v54, v55, 0xbfb8aa3b, v75
	ds_read_b32 v55, v150 offset:60
	s_nop 0
	v_add_f32_e32 v51, 1.0, v51
	v_rcp_f32_e32 v51, v51
	v_exp_f32_e32 v54, v54
	s_waitcnt lgkmcnt(0)
; __device__ __forceinline__ float fsigmoid(float x) { return __builtin_amdgcn_rcpf(1.f + __builtin_amdgcn_exp2f(-x * LOG2E)); }
; #define REC_SCAN_STEP(N_) asm volatile("s_nop 1\n\tv_fmac_f32_dpp %0, %0, %1 row_shr:" #N_ " row_mask:0xf bank_mask:0xf\n\ts_nop 1\n\tv_mul_f32_dpp %1, %1, %1 row_shr:" #N_ " row_mask:0xf bank_mask:0xf" : "+v"(bb), "+v"(a))
; __device__ __forceinline__ void rec1_unit(KArgs args, int L, int unit, LAS unsigned char* lds, int wave, int lane) {
;     ...
;             for (int e = 0; e < 8; ++e) {
;                 const int nn = e >> 2, jj = e & 3; const int cb = (32 * kh + 8 * q + e) * 8;
;                 const float xcv = (e & 1) ? bfhi(xw[e >> 1]) : bflo(xw[e >> 1]);
;                 const float r = fsigmoid(racc[nn][jj] + ct[cb + 5]), ig = fsigmoid(iacc[nn][jj] + ct[cb + 6]);
;                 float a = __builtin_amdgcn_exp2f(ct[cb + 7] * r);
;                 float bb = __builtin_amdgcn_sqrtf(fmaxf(1.f - a * a, 0.f)) * (ig * xcv);
;     ...
;                 REC_SCAN_STEP(1); REC_SCAN_STEP(2); REC_SCAN_STEP(4); REC_SCAN_STEP(8);
;     ...
;                 const float hl = a * Hcar[kh][e] + bb, ca = a * Acar[kh][e];
;                 hv[e] = hl; av[e] = ca;
;                 Hcar[kh][e] = __builtin_bit_cast(float, __builtin_amdgcn_ds_bpermute(bidx15, __builtin_bit_cast(int, hl))); Acar[kh][e] = __builtin_bit_cast(float, __builtin_amdgcn_ds_bpermute(bidx15, __builtin_bit_cast(int, ca)));
	v_mul_f32_e32 v51, v55, v51
	v_exp_f32_e32 v70, v51
	v_add_f32_e32 v54, 1.0, v54
	v_rcp_f32_e32 v54, v54
	v_fma_f32 v51, -v70, v70, 1.0
	v_max_f32_e32 v51, 0, v51
	v_sqrt_f32_e32 v51, v51
	v_mul_f32_e32 v50, v54, v50
	v_mul_f32_e32 v72, v50, v51
	s_nop 1
	v_fmac_f32_dpp v72, v72, v70 row_shr:1 row_mask:0xf bank_mask:0xf
	s_nop 1
	v_mul_f32_dpp v70, v70, v70 row_shr:1 row_mask:0xf bank_mask:0xf
	s_nop 0
	s_nop 1
	v_fmac_f32_dpp v72, v72, v70 row_shr:2 row_mask:0xf bank_mask:0xf
	s_nop 1
	v_mul_f32_dpp v70, v70, v70 row_shr:2 row_mask:0xf bank_mask:0xf
	s_nop 0
	s_nop 1
	v_fmac_f32_dpp v72, v72, v70 row_shr:4 row_mask:0xf bank_mask:0xf
	s_nop 1
	v_mul_f32_dpp v70, v70, v70 row_shr:4 row_mask:0xf bank_mask:0xf
	s_nop 0
	s_nop 1
	v_fmac_f32_dpp v72, v72, v70 row_shr:8 row_mask:0xf bank_mask:0xf
	s_nop 1
	v_mul_f32_dpp v70, v70, v70 row_shr:8 row_mask:0xf bank_mask:0xf
	s_nop 0
	v_pk_fma_f32 v[50:51], v[6:7], v[70:71], v[72:73]
	ds_bpermute_b32 v7, v149, v51
	v_pk_mul_f32 v[54:55], v[12:13], v[70:71]
	v_pk_mov_b32 v[70:71], v[50:51], v[50:51] op_sel:[1,0]
	ds_bpermute_b32 v6, v149, v50
	ds_read2_b32 v[50:51], v150 offset0:21 offset1:22
	v_pk_mov_b32 v[72:73], v[54:55], v[54:55] op_sel:[1,0]
	ds_bpermute_b32 v12, v149, v54
	v_lshlrev_b32_e32 v54, 16, v67
	ds_bpermute_b32 v13, v149, v55
	s_waitcnt lgkmcnt(2)
	v_fmamk_f32 v51, v56, 0xbfb8aa3b, v51
	v_fmamk_f32 v50, v52, 0xbfb8aa3b, v50
	s_nop 0
	s_nop 0
	v_exp_f32_e32 v51, v51
	v_exp_f32_e32 v50, v50
	v_add_f32_e32 v51, 1.0, v51
	v_add_f32_e32 v50, 1.0, v50
	v_rcp_f32_e32 v52, v51
	ds_read_b32 v51, v150 offset:92
	v_rcp_f32_e32 v50, v50
	v_mul_f32_e32 v52, v52, v54
	s_waitcnt lgkmcnt(0)
	v_mul_f32_e32 v50, v51, v50
	v_exp_f32_e32 v51, v50
	s_nop 0
	v_fma_f32 v50, -v51, v51, 1.0
	v_max_f32_e32 v50, 0, v50
	v_sqrt_f32_e32 v50, v50
	s_nop 0
	v_mul_f32_e32 v55, v52, v50
	s_nop 1
	v_fmac_f32_dpp v55, v55, v51 row_shr:1 row_mask:0xf bank_mask:0xf
	s_nop 1
	v_mul_f32_dpp v51, v51, v51 row_shr:1 row_mask:0xf bank_mask:0xf
	v_and_b32_e32 v52, 0xffff0000, v67
	s_nop 1
	v_fmac_f32_dpp v55, v55, v51 row_shr:2 row_mask:0xf bank_mask:0xf
	s_nop 1
	v_mul_f32_dpp v51, v51, v51 row_shr:2 row_mask:0xf bank_mask:0xf
	s_nop 0
	s_nop 1
	v_fmac_f32_dpp v55, v55, v51 row_shr:4 row_mask:0xf bank_mask:0xf
	s_nop 1
	v_mul_f32_dpp v51, v51, v51 row_shr:4 row_mask:0xf bank_mask:0xf
	s_nop 0
	s_nop 1
	v_fmac_f32_dpp v55, v55, v51 row_shr:8 row_mask:0xf bank_mask:0xf
	s_nop 1
	v_mul_f32_dpp v51, v51, v51 row_shr:8 row_mask:0xf bank_mask:0xf
	ds_read2_b32 v[74:75], v150 offset0:29 offset1:30
	ds_read_b32 v54, v150 offset:124
	s_waitcnt lgkmcnt(1)
	v_fmamk_f32 v50, v53, 0xbfb8aa3b, v74
	s_nop 0
	v_exp_f32_e32 v50, v50
	v_fmamk_f32 v53, v57, 0xbfb8aa3b, v75
	s_nop 0
	v_exp_f32_e32 v53, v53
	v_add_f32_e32 v50, 1.0, v50
	v_rcp_f32_e32 v50, v50
	v_add_f32_e32 v53, 1.0, v53
	v_rcp_f32_e32 v53, v53
	s_waitcnt lgkmcnt(0)
	v_mul_f32_e32 v50, v54, v50
	v_exp_f32_e32 v50, v50
	v_mul_f32_e32 v52, v53, v52
	v_fma_f32 v54, -v50, v50, 1.0
	v_max_f32_e32 v54, 0, v54
	v_sqrt_f32_e32 v54, v54
	s_nop 0
	v_mul_f32_e32 v54, v52, v54
	s_nop 1
	v_fmac_f32_dpp v54, v54, v50 row_shr:1 row_mask:0xf bank_mask:0xf
	s_nop 1
	v_mul_f32_dpp v50, v50, v50 row_shr:1 row_mask:0xf bank_mask:0xf
	s_nop 0
	s_nop 1
	v_fmac_f32_dpp v54, v54, v50 row_shr:2 row_mask:0xf bank_mask:0xf
	s_nop 1
	v_mul_f32_dpp v50, v50, v50 row_shr:2 row_mask:0xf bank_mask:0xf
	s_nop 0
	s_nop 1
	v_fmac_f32_dpp v54, v54, v50 row_shr:4 row_mask:0xf bank_mask:0xf
	s_nop 1
	v_mul_f32_dpp v50, v50, v50 row_shr:4 row_mask:0xf bank_mask:0xf
	s_nop 0
	s_nop 1
	v_fmac_f32_dpp v54, v54, v50 row_shr:8 row_mask:0xf bank_mask:0xf
	s_nop 1
	v_mul_f32_dpp v50, v50, v50 row_shr:8 row_mask:0xf bank_mask:0xf
	s_nop 0
	v_pk_fma_f32 v[52:53], v[138:139], v[50:51], v[54:55]
	v_pk_mul_f32 v[50:51], v[8:9], v[50:51]
	ds_bpermute_b32 v9, v149, v51
	v_pk_mov_b32 v[56:57], v[50:51], v[50:51] op_sel:[1,0]
	ds_bpermute_b32 v8, v149, v50
	ds_read2_b32 v[50:51], v150 offset0:37 offset1:38
	ds_bpermute_b32 v139, v149, v53
	v_pk_mov_b32 v[54:55], v[52:53], v[52:53] op_sel:[1,0]
	ds_bpermute_b32 v138, v149, v52
	v_lshlrev_b32_e32 v52, 16, v68
	s_waitcnt lgkmcnt(2)
	v_fmamk_f32 v51, v62, 0xbfb8aa3b, v51
	v_fmamk_f32 v50, v58, 0xbfb8aa3b, v50
	s_nop 0
	s_nop 0
	v_exp_f32_e32 v51, v51
	v_exp_f32_e32 v50, v50
	v_add_f32_e32 v51, 1.0, v51
	v_add_f32_e32 v50, 1.0, v50
	v_rcp_f32_e32 v53, v51
	ds_read_b32 v51, v150 offset:156
	v_rcp_f32_e32 v50, v50
	v_mul_f32_e32 v52, v53, v52
	s_waitcnt lgkmcnt(0)
	v_mul_f32_e32 v50, v51, v50
	v_exp_f32_e32 v51, v50
	s_nop 0
	v_fma_f32 v50, -v51, v51, 1.0
	v_max_f32_e32 v50, 0, v50
	v_sqrt_f32_e32 v50, v50
	s_nop 0
	v_mul_f32_e32 v53, v52, v50
	s_nop 1
	v_fmac_f32_dpp v53, v53, v51 row_shr:1 row_mask:0xf bank_mask:0xf
	s_nop 1
	v_mul_f32_dpp v51, v51, v51 row_shr:1 row_mask:0xf bank_mask:0xf
	v_and_b32_e32 v52, 0xffff0000, v68
	s_nop 1
	v_fmac_f32_dpp v53, v53, v51 row_shr:2 row_mask:0xf bank_mask:0xf
	s_nop 1
	v_mul_f32_dpp v51, v51, v51 row_shr:2 row_mask:0xf bank_mask:0xf
	s_nop 0
	s_nop 1
	v_fmac_f32_dpp v53, v53, v51 row_shr:4 row_mask:0xf bank_mask:0xf
	s_nop 1
	v_mul_f32_dpp v51, v51, v51 row_shr:4 row_mask:0xf bank_mask:0xf
	s_nop 0
	s_nop 1
	v_fmac_f32_dpp v53, v53, v51 row_shr:8 row_mask:0xf bank_mask:0xf
	s_nop 1
	v_mul_f32_dpp v51, v51, v51 row_shr:8 row_mask:0xf bank_mask:0xf
	ds_read2_b32 v[74:75], v150 offset0:45 offset1:46
	s_waitcnt lgkmcnt(0)
	v_fmamk_f32 v50, v59, 0xbfb8aa3b, v74
	s_nop 0
	v_exp_f32_e32 v50, v50
	ds_read_b32 v59, v150 offset:188
	v_fmamk_f32 v58, v63, 0xbfb8aa3b, v75
	s_nop 0
	v_add_f32_e32 v50, 1.0, v50
	v_rcp_f32_e32 v50, v50
	v_exp_f32_e32 v58, v58
	s_waitcnt lgkmcnt(0)
; __device__ __forceinline__ unsigned pk2(float lo, float hi) { const pk2_f32x2 v = {lo, hi}; return __builtin_bit_cast(unsigned, __builtin_convertvector(v, pk2_bf16x2)); }
; __device__ __forceinline__ float fsigmoid(float x) { return __builtin_amdgcn_rcpf(1.f + __builtin_amdgcn_exp2f(-x * LOG2E)); }
; #define REC_SCAN_STEP(N_) asm volatile("s_nop 1\n\tv_fmac_f32_dpp %0, %0, %1 row_shr:" #N_ " row_mask:0xf bank_mask:0xf\n\ts_nop 1\n\tv_mul_f32_dpp %1, %1, %1 row_shr:" #N_ " row_mask:0xf bank_mask:0xf" : "+v"(bb), "+v"(a))
; __device__ __forceinline__ void rec1_unit(KArgs args, int L, int unit, LAS unsigned char* lds, int wave, int lane) {
;     ...
;             for (int e = 0; e < 8; ++e) {
;                 const int nn = e >> 2, jj = e & 3; const int cb = (32 * kh + 8 * q + e) * 8;
;                 const float xcv = (e & 1) ? bfhi(xw[e >> 1]) : bflo(xw[e >> 1]);
;                 const float r = fsigmoid(racc[nn][jj] + ct[cb + 5]), ig = fsigmoid(iacc[nn][jj] + ct[cb + 6]);
;                 float a = __builtin_amdgcn_exp2f(ct[cb + 7] * r);
;                 float bb = __builtin_amdgcn_sqrtf(fmaxf(1.f - a * a, 0.f)) * (ig * xcv);
;     ...
;                 REC_SCAN_STEP(1); REC_SCAN_STEP(2); REC_SCAN_STEP(4); REC_SCAN_STEP(8);
;     ...
;                 const float hl = a * Hcar[kh][e] + bb, ca = a * Acar[kh][e];
;                 hv[e] = hl; av[e] = ca;
;                 Hcar[kh][e] = __builtin_bit_cast(float, __builtin_amdgcn_ds_bpermute(bidx15, __builtin_bit_cast(int, hl))); Acar[kh][e] = __builtin_bit_cast(float, __builtin_amdgcn_ds_bpermute(bidx15, __builtin_bit_cast(int, ca)));
;             }
;             const size_t o = (size_t)(b * SEQ + t) * D_REC + 64 * hb + 32 * kh + 8 * q;
;             u32x4 w; w.x = pk2(hv[0], hv[1]); w.y = pk2(hv[2], hv[3]); w.z = pk2(hv[4], hv[5]); w.w = pk2(hv[6], hv[7]);
;             *(u32x4*)(hloc + o) = w;
;             w.x = pk2(av[0], av[1]); w.y = pk2(av[2], av[3]); w.z = pk2(av[4], av[5]); w.w = pk2(av[6], av[7]);
;             *(u32x4*)(cumA + o) = w;
	v_mul_f32_e32 v50, v59, v50
	v_exp_f32_e32 v50, v50
	v_add_f32_e32 v58, 1.0, v58
	v_rcp_f32_e32 v58, v58
	v_fma_f32 v59, -v50, v50, 1.0
	v_max_f32_e32 v59, 0, v59
	v_sqrt_f32_e32 v59, v59
	v_mul_f32_e32 v52, v58, v52
	v_mul_f32_e32 v52, v52, v59
	s_nop 1
	v_fmac_f32_dpp v52, v52, v50 row_shr:1 row_mask:0xf bank_mask:0xf
	s_nop 1
	v_mul_f32_dpp v50, v50, v50 row_shr:1 row_mask:0xf bank_mask:0xf
	s_nop 0
	s_nop 1
	v_fmac_f32_dpp v52, v52, v50 row_shr:2 row_mask:0xf bank_mask:0xf
	s_nop 1
	v_mul_f32_dpp v50, v50, v50 row_shr:2 row_mask:0xf bank_mask:0xf
	s_nop 0
	s_nop 1
	v_fmac_f32_dpp v52, v52, v50 row_shr:4 row_mask:0xf bank_mask:0xf
	s_nop 1
	v_mul_f32_dpp v50, v50, v50 row_shr:4 row_mask:0xf bank_mask:0xf
	s_nop 0
	s_nop 1
	v_fmac_f32_dpp v52, v52, v50 row_shr:8 row_mask:0xf bank_mask:0xf
	s_nop 1
	v_mul_f32_dpp v50, v50, v50 row_shr:8 row_mask:0xf bank_mask:0xf
	s_nop 0
	v_pk_fma_f32 v[52:53], v[134:135], v[50:51], v[52:53]
	v_pk_mul_f32 v[50:51], v[4:5], v[50:51]
	ds_bpermute_b32 v5, v149, v51
	v_pk_mov_b32 v[62:63], v[50:51], v[50:51] op_sel:[1,0]
	ds_bpermute_b32 v4, v149, v50
	ds_read2_b32 v[50:51], v150 offset0:53 offset1:54
	ds_bpermute_b32 v135, v149, v53
	v_pk_mov_b32 v[58:59], v[52:53], v[52:53] op_sel:[1,0]
	ds_bpermute_b32 v134, v149, v52
	v_lshlrev_b32_e32 v52, 16, v69
	s_waitcnt lgkmcnt(2)
	v_fmamk_f32 v51, v64, 0xbfb8aa3b, v51
	v_fmamk_f32 v50, v60, 0xbfb8aa3b, v50
	s_nop 0
	s_nop 0
	v_exp_f32_e32 v51, v51
	v_exp_f32_e32 v50, v50
	v_add_f32_e32 v51, 1.0, v51
	v_add_f32_e32 v50, 1.0, v50
	v_rcp_f32_e32 v53, v51
	ds_read_b32 v51, v150 offset:220
	v_rcp_f32_e32 v50, v50
	v_mul_f32_e32 v52, v53, v52
	s_waitcnt lgkmcnt(0)
	v_mul_f32_e32 v50, v51, v50
	v_exp_f32_e32 v51, v50
	s_nop 0
	v_fma_f32 v50, -v51, v51, 1.0
	v_max_f32_e32 v50, 0, v50
	v_sqrt_f32_e32 v50, v50
	s_nop 0
	v_mul_f32_e32 v53, v52, v50
	s_nop 1
	v_fmac_f32_dpp v53, v53, v51 row_shr:1 row_mask:0xf bank_mask:0xf
	s_nop 1
	v_mul_f32_dpp v51, v51, v51 row_shr:1 row_mask:0xf bank_mask:0xf
	v_and_b32_e32 v52, 0xffff0000, v69
	s_nop 1
	v_fmac_f32_dpp v53, v53, v51 row_shr:2 row_mask:0xf bank_mask:0xf
	s_nop 1
	v_mul_f32_dpp v51, v51, v51 row_shr:2 row_mask:0xf bank_mask:0xf
	s_nop 0
	s_nop 1
	v_fmac_f32_dpp v53, v53, v51 row_shr:4 row_mask:0xf bank_mask:0xf
	s_nop 1
	v_mul_f32_dpp v51, v51, v51 row_shr:4 row_mask:0xf bank_mask:0xf
	s_nop 0
	s_nop 1
	v_fmac_f32_dpp v53, v53, v51 row_shr:8 row_mask:0xf bank_mask:0xf
	s_nop 1
	v_mul_f32_dpp v51, v51, v51 row_shr:8 row_mask:0xf bank_mask:0xf
	ds_read2_b32 v[74:75], v150 offset0:61 offset1:62
	s_waitcnt lgkmcnt(0)
	v_fmamk_f32 v50, v61, 0xbfb8aa3b, v74
	s_nop 0
	v_exp_f32_e32 v50, v50
	ds_read_b32 v61, v150 offset:252
	v_fmamk_f32 v60, v65, 0xbfb8aa3b, v75
	s_nop 0
	v_add_f32_e32 v50, 1.0, v50
	v_rcp_f32_e32 v50, v50
	v_exp_f32_e32 v60, v60
	s_waitcnt vmcnt(7)
	v_mov_b64_e32 v[76:77], v[16:17]
	v_mov_b64_e32 v[74:75], v[14:15]
	s_waitcnt lgkmcnt(0)
	v_mul_f32_e32 v50, v61, v50
	v_exp_f32_e32 v50, v50
	v_add_f32_e32 v60, 1.0, v60
	v_rcp_f32_e32 v60, v60
	v_fma_f32 v61, -v50, v50, 1.0
	v_max_f32_e32 v61, 0, v61
	v_sqrt_f32_e32 v61, v61
	v_mul_f32_e32 v52, v60, v52
	v_mov_b32_e32 v60, v51
	v_mul_f32_e32 v52, v52, v61
	s_nop 1
	v_fmac_f32_dpp v52, v52, v50 row_shr:1 row_mask:0xf bank_mask:0xf
	s_nop 1
	v_mul_f32_dpp v50, v50, v50 row_shr:1 row_mask:0xf bank_mask:0xf
	s_nop 0
	s_nop 1
	v_fmac_f32_dpp v52, v52, v50 row_shr:2 row_mask:0xf bank_mask:0xf
	s_nop 1
	v_mul_f32_dpp v50, v50, v50 row_shr:2 row_mask:0xf bank_mask:0xf
	s_nop 0
	s_nop 1
	v_fmac_f32_dpp v52, v52, v50 row_shr:4 row_mask:0xf bank_mask:0xf
	s_nop 1
	v_mul_f32_dpp v50, v50, v50 row_shr:4 row_mask:0xf bank_mask:0xf
	s_nop 0
	s_nop 1
	v_fmac_f32_dpp v52, v52, v50 row_shr:8 row_mask:0xf bank_mask:0xf
	s_nop 1
	v_mul_f32_dpp v50, v50, v50 row_shr:8 row_mask:0xf bank_mask:0xf
	s_nop 0
	v_pk_fma_f32 v[52:53], v[128:129], v[50:51], v[52:53]
	v_mov_b32_e32 v61, v50
	v_pk_mov_b32 v[64:65], v[52:53], v[52:53] op_sel:[1,0]
	ds_bpermute_b32 v129, v149, v53
	v_pk_mul_f32 v[60:61], v[136:137], v[60:61]
	ds_bpermute_b32 v128, v149, v52
	v_cvt_pk_bf16_f32 v50, v70, v71
	v_cvt_pk_bf16_f32 v51, v54, v55
	v_cvt_pk_bf16_f32 v52, v58, v59
	v_cvt_pk_bf16_f32 v53, v64, v65
	v_lshl_add_u64 v[54:55], s[6:7], 0, v[10:11]
	global_store_dwordx4 v[54:55], v[50:53], off
	v_lshl_add_u64 v[54:55], s[18:19], 0, v[10:11]
	ds_bpermute_b32 v136, v149, v60
	v_cvt_pk_bf16_f32 v50, v72, v73
	v_cvt_pk_bf16_f32 v51, v56, v57
	v_cvt_pk_bf16_f32 v52, v62, v63
	v_cvt_pk_bf16_f32 v53, v60, v61
	global_store_dwordx4 v[54:55], v[50:53], off
	ds_read_b128 v[50:53], v146 offset:4096
	ds_read_b128 v[54:57], v146 offset:12288
	ds_bpermute_b32 v137, v149, v61
	ds_read_b128 v[58:61], v146 offset:5120
	ds_read_b128 v[70:73], v146 offset:13312
	s_waitcnt lgkmcnt(4)
	v_mfma_f32_16x16x32_bf16 v[50:53], v[50:53], v[66:69], 0
	v_or_b32_e32 v10, 64, v10
	s_waitcnt lgkmcnt(3)
	v_mfma_f32_16x16x32_bf16 v[54:57], v[54:57], v[66:69], 0
	s_waitcnt lgkmcnt(1)
	v_mfma_f32_16x16x32_bf16 v[62:65], v[58:61], v[46:49], v[50:53]
	s_waitcnt lgkmcnt(0)
	v_mfma_f32_16x16x32_bf16 v[58:61], v[70:73], v[46:49], v[54:57]
	s_nop 0
	ds_read_b128 v[50:53], v146 offset:6144
	s_nop 1
	ds_read_b128 v[54:57], v146 offset:14336
	s_waitcnt lgkmcnt(1)
	v_mfma_f32_16x16x32_bf16 v[50:53], v[50:53], v[66:69], 0
	s_waitcnt lgkmcnt(0)
	v_mfma_f32_16x16x32_bf16 v[66:69], v[54:57], v[66:69], 0
	ds_read_b128 v[54:57], v146 offset:7168
	ds_read_b128 v[70:73], v146 offset:15360
	s_waitcnt lgkmcnt(1)
	v_mfma_f32_16x16x32_bf16 v[54:57], v[54:57], v[46:49], v[50:53]
	s_waitcnt lgkmcnt(0)
; #define LAS __attribute__((address_space(3)))
; __device__ __forceinline__ float fsigmoid(float x) { return __builtin_amdgcn_rcpf(1.f + __builtin_amdgcn_exp2f(-x * LOG2E)); }
; #define REC_SCAN_STEP(N_) asm volatile("s_nop 1\n\tv_fmac_f32_dpp %0, %0, %1 row_shr:" #N_ " row_mask:0xf bank_mask:0xf\n\ts_nop 1\n\tv_mul_f32_dpp %1, %1, %1 row_shr:" #N_ " row_mask:0xf bank_mask:0xf" : "+v"(bb), "+v"(a))
; __device__ __forceinline__ void rec1_unit(KArgs args, int L, int unit, LAS unsigned char* lds, int wave, int lane) {
;     ...
;         for (int kh = 0; kh < 2; ++kh) {
;             f32x4 racc[2], iacc[2];
; #pragma unroll
;             for (int nn = 0; nn < 2; ++nn) { racc[nn] = (f32x4){0.f, 0.f, 0.f, 0.f}; iacc[nn] = (f32x4){0.f, 0.f, 0.f, 0.f};
; #pragma unroll
;                 for (int kk = 0; kk < 2; ++kk) { const int n = 2 * kh + nn;
;                     const bf16x8 fa = *(const LAS bf16x8*)(wl + ((0 * 4 + n) * 2 + kk) * 1024 + lane * 16), fx = *(const LAS bf16x8*)(wl + ((1 * 4 + n) * 2 + kk) * 1024 + lane * 16);
;                     const bf16x8 xk = __builtin_bit_cast(bf16x8, xb[kk]);
;                     racc[nn] = __builtin_amdgcn_mfma_f32_16x16x32_bf16(fa, xk, racc[nn], 0, 0, 0); iacc[nn] = __builtin_amdgcn_mfma_f32_16x16x32_bf16(fx, xk, iacc[nn], 0, 0, 0); } }
;             const unsigned xw[4] = {xb[kh].x, xb[kh].y, xb[kh].z, xb[kh].w};
;             float hv[8], av[8];
; #pragma unroll
;             for (int e = 0; e < 8; ++e) {
;                 const int nn = e >> 2, jj = e & 3; const int cb = (32 * kh + 8 * q + e) * 8;
;                 const float xcv = (e & 1) ? bfhi(xw[e >> 1]) : bflo(xw[e >> 1]);
;                 const float r = fsigmoid(racc[nn][jj] + ct[cb + 5]), ig = fsigmoid(iacc[nn][jj] + ct[cb + 6]);
;                 float a = __builtin_amdgcn_exp2f(ct[cb + 7] * r);
;                 float bb = __builtin_amdgcn_sqrtf(fmaxf(1.f - a * a, 0.f)) * (ig * xcv);
;     ...
;                 REC_SCAN_STEP(1); REC_SCAN_STEP(2); REC_SCAN_STEP(4); REC_SCAN_STEP(8);
;     ...
;                 const float hl = a * Hcar[kh][e] + bb, ca = a * Acar[kh][e];
;                 hv[e] = hl; av[e] = ca;
;                 Hcar[kh][e] = __builtin_bit_cast(float, __builtin_amdgcn_ds_bpermute(bidx15, __builtin_bit_cast(int, hl))); Acar[kh][e] = __builtin_bit_cast(float, __builtin_amdgcn_ds_bpermute(bidx15, __builtin_bit_cast(int, ca)));
	v_mfma_f32_16x16x32_bf16 v[50:53], v[70:73], v[46:49], v[66:69]
	s_nop 2
	v_add_u32_e32 v67, 0x414, v150
	ds_read2_b32 v[68:69], v67 offset1:1
	ds_read_b32 v67, v150 offset:1052
	v_lshlrev_b32_e32 v66, 16, v46
	v_and_b32_e32 v46, 0xffff0000, v46
	s_waitcnt lgkmcnt(1)
	v_fmamk_f32 v62, v62, 0xbfb8aa3b, v68
	s_nop 0
	v_exp_f32_e32 v62, v62
	v_fmamk_f32 v58, v58, 0xbfb8aa3b, v69
	s_nop 0
	v_exp_f32_e32 v58, v58
	v_add_f32_e32 v62, 1.0, v62
	v_rcp_f32_e32 v62, v62
	v_add_f32_e32 v58, 1.0, v58
	v_rcp_f32_e32 v58, v58
	s_waitcnt lgkmcnt(0)
	v_mul_f32_e32 v62, v67, v62
	v_exp_f32_e32 v67, v62
	v_mul_f32_e32 v58, v58, v66
	v_fma_f32 v62, -v67, v67, 1.0
	v_max_f32_e32 v62, 0, v62
	v_sqrt_f32_e32 v62, v62
	s_nop 0
	v_mul_f32_e32 v69, v58, v62
	s_nop 1
	v_fmac_f32_dpp v69, v69, v67 row_shr:1 row_mask:0xf bank_mask:0xf
	s_nop 1
	v_mul_f32_dpp v67, v67, v67 row_shr:1 row_mask:0xf bank_mask:0xf
	v_add_u32_e32 v58, 0x434, v150
	s_nop 1
	v_fmac_f32_dpp v69, v69, v67 row_shr:2 row_mask:0xf bank_mask:0xf
	s_nop 1
	v_mul_f32_dpp v67, v67, v67 row_shr:2 row_mask:0xf bank_mask:0xf
	s_nop 0
	s_nop 1
	v_fmac_f32_dpp v69, v69, v67 row_shr:4 row_mask:0xf bank_mask:0xf
	s_nop 1
	v_mul_f32_dpp v67, v67, v67 row_shr:4 row_mask:0xf bank_mask:0xf
	s_nop 0
	s_nop 1
	v_fmac_f32_dpp v69, v69, v67 row_shr:8 row_mask:0xf bank_mask:0xf
	s_nop 1
	v_mul_f32_dpp v67, v67, v67 row_shr:8 row_mask:0xf bank_mask:0xf
	ds_read2_b32 v[70:71], v58 offset1:1
	ds_read_b32 v62, v150 offset:1084
	s_waitcnt lgkmcnt(1)
	v_fmamk_f32 v58, v63, 0xbfb8aa3b, v70
	s_nop 0
	v_exp_f32_e32 v58, v58
	v_fmamk_f32 v59, v59, 0xbfb8aa3b, v71
	s_nop 0
	v_exp_f32_e32 v59, v59
	v_add_f32_e32 v58, 1.0, v58
	v_rcp_f32_e32 v58, v58
	s_waitcnt vmcnt(8)
	v_mov_b64_e32 v[72:73], v[20:21]
	v_add_f32_e32 v59, 1.0, v59
	v_rcp_f32_e32 v59, v59
	s_waitcnt lgkmcnt(0)
	v_mul_f32_e32 v58, v62, v58
	v_exp_f32_e32 v66, v58
	v_mov_b64_e32 v[70:71], v[18:19]
	v_mul_f32_e32 v46, v59, v46
	v_fma_f32 v58, -v66, v66, 1.0
	v_max_f32_e32 v58, 0, v58
	v_sqrt_f32_e32 v58, v58
	s_nop 0
	v_mul_f32_e32 v68, v46, v58
	s_nop 1
	v_fmac_f32_dpp v68, v68, v66 row_shr:1 row_mask:0xf bank_mask:0xf
	s_nop 1
	v_mul_f32_dpp v66, v66, v66 row_shr:1 row_mask:0xf bank_mask:0xf
	v_mov_b32_e32 v58, v67
	s_nop 1
	v_fmac_f32_dpp v68, v68, v66 row_shr:2 row_mask:0xf bank_mask:0xf
	s_nop 1
	v_mul_f32_dpp v66, v66, v66 row_shr:2 row_mask:0xf bank_mask:0xf
	v_lshlrev_b32_e32 v46, 16, v47
	s_nop 1
	v_fmac_f32_dpp v68, v68, v66 row_shr:4 row_mask:0xf bank_mask:0xf
	s_nop 1
	v_mul_f32_dpp v66, v66, v66 row_shr:4 row_mask:0xf bank_mask:0xf
	s_nop 0
	s_nop 1
	v_fmac_f32_dpp v68, v68, v66 row_shr:8 row_mask:0xf bank_mask:0xf
	s_nop 1
	v_mul_f32_dpp v66, v66, v66 row_shr:8 row_mask:0xf bank_mask:0xf
	s_nop 0
	v_pk_fma_f32 v[68:69], v[122:123], v[66:67], v[68:69]
	v_mov_b32_e32 v59, v66
	v_add_u32_e32 v66, 0x454, v150
	ds_read2_b32 v[66:67], v66 offset1:1
	ds_bpermute_b32 v123, v149, v69
	v_pk_mov_b32 v[62:63], v[68:69], v[68:69] op_sel:[1,0]
	ds_bpermute_b32 v122, v149, v68
	v_pk_mul_f32 v[58:59], v[132:133], v[58:59]
	s_waitcnt lgkmcnt(2)
	v_fmamk_f32 v64, v64, 0xbfb8aa3b, v66
	s_nop 0
	v_exp_f32_e32 v64, v64
	ds_read_b32 v66, v150 offset:1116
	v_fmamk_f32 v60, v60, 0xbfb8aa3b, v67
	s_nop 0
	v_add_f32_e32 v64, 1.0, v64
	v_rcp_f32_e32 v64, v64
	v_exp_f32_e32 v60, v60
	ds_bpermute_b32 v132, v149, v58
	ds_bpermute_b32 v133, v149, v59
	s_waitcnt lgkmcnt(2)
	v_mul_f32_e32 v64, v66, v64
	v_exp_f32_e32 v67, v64
	v_add_f32_e32 v60, 1.0, v60
	v_rcp_f32_e32 v60, v60
	v_fma_f32 v64, -v67, v67, 1.0
	v_max_f32_e32 v64, 0, v64
	v_sqrt_f32_e32 v64, v64
	v_mul_f32_e32 v46, v60, v46
	v_and_b32_e32 v60, 0xffff0000, v47
	v_mul_f32_e32 v69, v46, v64
	s_nop 1
	v_fmac_f32_dpp v69, v69, v67 row_shr:1 row_mask:0xf bank_mask:0xf
	s_nop 1
	v_mul_f32_dpp v67, v67, v67 row_shr:1 row_mask:0xf bank_mask:0xf
	v_add_u32_e32 v46, 0x474, v150
	s_nop 1
	v_fmac_f32_dpp v69, v69, v67 row_shr:2 row_mask:0xf bank_mask:0xf
	s_nop 1
	v_mul_f32_dpp v67, v67, v67 row_shr:2 row_mask:0xf bank_mask:0xf
	s_nop 0
	s_nop 1
	v_fmac_f32_dpp v69, v69, v67 row_shr:4 row_mask:0xf bank_mask:0xf
	s_nop 1
	v_mul_f32_dpp v67, v67, v67 row_shr:4 row_mask:0xf bank_mask:0xf
	s_nop 0
	s_nop 1
	v_fmac_f32_dpp v69, v69, v67 row_shr:8 row_mask:0xf bank_mask:0xf
	s_nop 1
	v_mul_f32_dpp v67, v67, v67 row_shr:8 row_mask:0xf bank_mask:0xf
	ds_read2_b32 v[46:47], v46 offset1:1
	s_waitcnt lgkmcnt(0)
	v_fmamk_f32 v46, v65, 0xbfb8aa3b, v46
	s_nop 0
	v_exp_f32_e32 v46, v46
	v_fmamk_f32 v47, v61, 0xbfb8aa3b, v47
	ds_read_b32 v61, v150 offset:1148
	s_nop 0
	v_add_f32_e32 v46, 1.0, v46
	v_rcp_f32_e32 v46, v46
	v_exp_f32_e32 v47, v47
	s_waitcnt lgkmcnt(0)
	v_mul_f32_e32 v46, v61, v46
	v_exp_f32_e32 v66, v46
	v_add_f32_e32 v47, 1.0, v47
	v_rcp_f32_e32 v47, v47
	v_fma_f32 v46, -v66, v66, 1.0
	v_max_f32_e32 v46, 0, v46
	v_sqrt_f32_e32 v46, v46
	v_mul_f32_e32 v47, v47, v60
	v_mul_f32_e32 v68, v47, v46
	s_nop 1
	v_fmac_f32_dpp v68, v68, v66 row_shr:1 row_mask:0xf bank_mask:0xf
	s_nop 1
	v_mul_f32_dpp v66, v66, v66 row_shr:1 row_mask:0xf bank_mask:0xf
	v_mov_b32_e32 v46, v67
	s_nop 1
	v_fmac_f32_dpp v68, v68, v66 row_shr:2 row_mask:0xf bank_mask:0xf
	s_nop 1
	v_mul_f32_dpp v66, v66, v66 row_shr:2 row_mask:0xf bank_mask:0xf
	s_nop 0
	s_nop 1
	v_fmac_f32_dpp v68, v68, v66 row_shr:4 row_mask:0xf bank_mask:0xf
	s_nop 1
	v_mul_f32_dpp v66, v66, v66 row_shr:4 row_mask:0xf bank_mask:0xf
	s_nop 0
	s_nop 1
	v_fmac_f32_dpp v68, v68, v66 row_shr:8 row_mask:0xf bank_mask:0xf
	s_nop 1
	v_mul_f32_dpp v66, v66, v66 row_shr:8 row_mask:0xf bank_mask:0xf
	s_nop 0
	v_pk_fma_f32 v[64:65], v[120:121], v[66:67], v[68:69]
	ds_bpermute_b32 v120, v149, v64
	v_pk_mov_b32 v[60:61], v[64:65], v[64:65] op_sel:[1,0]
	v_add_u32_e32 v64, 0x494, v150
	ds_bpermute_b32 v121, v149, v65
	ds_read2_b32 v[64:65], v64 offset1:1
	v_mov_b32_e32 v47, v66
	v_lshlrev_b32_e32 v66, 16, v48
	v_and_b32_e32 v48, 0xffff0000, v48
	v_pk_mul_f32 v[46:47], v[130:131], v[46:47]
	s_waitcnt lgkmcnt(0)
; __device__ __forceinline__ unsigned pk2(float lo, float hi) { const pk2_f32x2 v = {lo, hi}; return __builtin_bit_cast(unsigned, __builtin_convertvector(v, pk2_bf16x2)); }
; __device__ __forceinline__ float fsigmoid(float x) { return __builtin_amdgcn_rcpf(1.f + __builtin_amdgcn_exp2f(-x * LOG2E)); }
; #define REC_SCAN_STEP(N_) asm volatile("s_nop 1\n\tv_fmac_f32_dpp %0, %0, %1 row_shr:" #N_ " row_mask:0xf bank_mask:0xf\n\ts_nop 1\n\tv_mul_f32_dpp %1, %1, %1 row_shr:" #N_ " row_mask:0xf bank_mask:0xf" : "+v"(bb), "+v"(a))
; __device__ __forceinline__ void rec1_unit(KArgs args, int L, int unit, LAS unsigned char* lds, int wave, int lane) {
;     ...
;             for (int e = 0; e < 8; ++e) {
;                 const int nn = e >> 2, jj = e & 3; const int cb = (32 * kh + 8 * q + e) * 8;
;                 const float xcv = (e & 1) ? bfhi(xw[e >> 1]) : bflo(xw[e >> 1]);
;                 const float r = fsigmoid(racc[nn][jj] + ct[cb + 5]), ig = fsigmoid(iacc[nn][jj] + ct[cb + 6]);
;                 float a = __builtin_amdgcn_exp2f(ct[cb + 7] * r);
;                 float bb = __builtin_amdgcn_sqrtf(fmaxf(1.f - a * a, 0.f)) * (ig * xcv);
;     ...
;                 REC_SCAN_STEP(1); REC_SCAN_STEP(2); REC_SCAN_STEP(4); REC_SCAN_STEP(8);
;     ...
;                 const float hl = a * Hcar[kh][e] + bb, ca = a * Acar[kh][e];
;                 hv[e] = hl; av[e] = ca;
;                 Hcar[kh][e] = __builtin_bit_cast(float, __builtin_amdgcn_ds_bpermute(bidx15, __builtin_bit_cast(int, hl))); Acar[kh][e] = __builtin_bit_cast(float, __builtin_amdgcn_ds_bpermute(bidx15, __builtin_bit_cast(int, ca)));
;             }
;             const size_t o = (size_t)(b * SEQ + t) * D_REC + 64 * hb + 32 * kh + 8 * q;
;             u32x4 w; w.x = pk2(hv[0], hv[1]); w.y = pk2(hv[2], hv[3]); w.z = pk2(hv[4], hv[5]); w.w = pk2(hv[6], hv[7]);
;             *(u32x4*)(hloc + o) = w;
;             w.x = pk2(av[0], av[1]); w.y = pk2(av[2], av[3]); w.z = pk2(av[4], av[5]); w.w = pk2(av[6], av[7]);
;             *(u32x4*)(cumA + o) = w;
;             asm volatile("" ::: "memory");
;         }
; #pragma unroll
;         for (int kk = 0; kk < 2; ++kk)
; #pragma unroll
;             for (int j = 0; j < 4; ++j) rawc[kk][j] = rawn[kk][j];
	v_fmamk_f32 v54, v54, 0xbfb8aa3b, v64
	s_nop 0
	v_exp_f32_e32 v54, v54
	ds_read_b32 v64, v150 offset:1180
	v_fmamk_f32 v50, v50, 0xbfb8aa3b, v65
	s_nop 0
	v_add_f32_e32 v54, 1.0, v54
	v_rcp_f32_e32 v54, v54
	v_exp_f32_e32 v50, v50
	ds_bpermute_b32 v130, v149, v46
	ds_bpermute_b32 v131, v149, v47
	s_waitcnt lgkmcnt(2)
	v_mul_f32_e32 v54, v64, v54
	v_exp_f32_e32 v65, v54
	v_add_f32_e32 v50, 1.0, v50
	v_rcp_f32_e32 v50, v50
	v_fma_f32 v54, -v65, v65, 1.0
	v_max_f32_e32 v54, 0, v54
	v_sqrt_f32_e32 v54, v54
	v_mul_f32_e32 v50, v50, v66
	v_mul_f32_e32 v67, v50, v54
	s_nop 1
	v_fmac_f32_dpp v67, v67, v65 row_shr:1 row_mask:0xf bank_mask:0xf
	s_nop 1
	v_mul_f32_dpp v65, v65, v65 row_shr:1 row_mask:0xf bank_mask:0xf
	v_add_u32_e32 v50, 0x4b4, v150
	s_nop 1
	v_fmac_f32_dpp v67, v67, v65 row_shr:2 row_mask:0xf bank_mask:0xf
	s_nop 1
	v_mul_f32_dpp v65, v65, v65 row_shr:2 row_mask:0xf bank_mask:0xf
	s_nop 0
	s_nop 1
	v_fmac_f32_dpp v67, v67, v65 row_shr:4 row_mask:0xf bank_mask:0xf
	s_nop 1
	v_mul_f32_dpp v65, v65, v65 row_shr:4 row_mask:0xf bank_mask:0xf
	s_nop 0
	s_nop 1
	v_fmac_f32_dpp v67, v67, v65 row_shr:8 row_mask:0xf bank_mask:0xf
	s_nop 1
	v_mul_f32_dpp v65, v65, v65 row_shr:8 row_mask:0xf bank_mask:0xf
	ds_read2_b32 v[68:69], v50 offset1:1
	ds_read_b32 v54, v150 offset:1212
	s_waitcnt lgkmcnt(1)
	v_fmamk_f32 v50, v55, 0xbfb8aa3b, v68
	s_nop 0
	v_exp_f32_e32 v50, v50
	v_fmamk_f32 v51, v51, 0xbfb8aa3b, v69
	s_nop 0
	v_exp_f32_e32 v51, v51
	v_add_f32_e32 v50, 1.0, v50
	v_rcp_f32_e32 v50, v50
	v_add_f32_e32 v51, 1.0, v51
	v_rcp_f32_e32 v51, v51
	s_waitcnt lgkmcnt(0)
	v_mul_f32_e32 v50, v54, v50
	v_exp_f32_e32 v64, v50
	v_mul_f32_e32 v48, v51, v48
	v_fma_f32 v50, -v64, v64, 1.0
	v_max_f32_e32 v50, 0, v50
	v_sqrt_f32_e32 v50, v50
	s_nop 0
	v_mul_f32_e32 v66, v48, v50
	s_nop 1
	v_fmac_f32_dpp v66, v66, v64 row_shr:1 row_mask:0xf bank_mask:0xf
	s_nop 1
	v_mul_f32_dpp v64, v64, v64 row_shr:1 row_mask:0xf bank_mask:0xf
	v_mov_b32_e32 v50, v65
	s_nop 1
	v_fmac_f32_dpp v66, v66, v64 row_shr:2 row_mask:0xf bank_mask:0xf
	s_nop 1
	v_mul_f32_dpp v64, v64, v64 row_shr:2 row_mask:0xf bank_mask:0xf
	v_lshlrev_b32_e32 v48, 16, v49
	s_nop 1
	v_fmac_f32_dpp v66, v66, v64 row_shr:4 row_mask:0xf bank_mask:0xf
	s_nop 1
	v_mul_f32_dpp v64, v64, v64 row_shr:4 row_mask:0xf bank_mask:0xf
	s_nop 0
	s_nop 1
	v_fmac_f32_dpp v66, v66, v64 row_shr:8 row_mask:0xf bank_mask:0xf
	s_nop 1
	v_mul_f32_dpp v64, v64, v64 row_shr:8 row_mask:0xf bank_mask:0xf
	s_nop 0
	v_pk_fma_f32 v[66:67], v[118:119], v[64:65], v[66:67]
	v_mov_b32_e32 v51, v64
	v_add_u32_e32 v64, 0x4d4, v150
	ds_read2_b32 v[64:65], v64 offset1:1
	ds_bpermute_b32 v119, v149, v67
	v_pk_mov_b32 v[54:55], v[66:67], v[66:67] op_sel:[1,0]
	ds_bpermute_b32 v118, v149, v66
	v_pk_mul_f32 v[50:51], v[126:127], v[50:51]
	s_waitcnt lgkmcnt(2)
	v_fmamk_f32 v56, v56, 0xbfb8aa3b, v64
	s_nop 0
	v_exp_f32_e32 v56, v56
	ds_read_b32 v64, v150 offset:1244
	v_fmamk_f32 v52, v52, 0xbfb8aa3b, v65
	s_nop 0
	v_add_f32_e32 v56, 1.0, v56
	v_rcp_f32_e32 v56, v56
	v_exp_f32_e32 v52, v52
	v_cvt_pk_bf16_f32 v54, v54, v55
	ds_bpermute_b32 v126, v149, v50
	s_waitcnt lgkmcnt(1)
	v_mul_f32_e32 v56, v64, v56
	v_exp_f32_e32 v65, v56
	v_add_f32_e32 v52, 1.0, v52
	v_rcp_f32_e32 v52, v52
	ds_bpermute_b32 v127, v149, v51
	v_fma_f32 v56, -v65, v65, 1.0
	v_max_f32_e32 v56, 0, v56
	v_sqrt_f32_e32 v56, v56
	v_mul_f32_e32 v48, v52, v48
	v_and_b32_e32 v52, 0xffff0000, v49
	v_cvt_pk_bf16_f32 v50, v50, v51
	v_mul_f32_e32 v67, v48, v56
	s_nop 1
	v_fmac_f32_dpp v67, v67, v65 row_shr:1 row_mask:0xf bank_mask:0xf
	s_nop 1
	v_mul_f32_dpp v65, v65, v65 row_shr:1 row_mask:0xf bank_mask:0xf
	v_add_u32_e32 v48, 0x4f4, v150
	s_nop 1
	v_fmac_f32_dpp v67, v67, v65 row_shr:2 row_mask:0xf bank_mask:0xf
	s_nop 1
	v_mul_f32_dpp v65, v65, v65 row_shr:2 row_mask:0xf bank_mask:0xf
	s_nop 0
	s_nop 1
	v_fmac_f32_dpp v67, v67, v65 row_shr:4 row_mask:0xf bank_mask:0xf
	s_nop 1
	v_mul_f32_dpp v65, v65, v65 row_shr:4 row_mask:0xf bank_mask:0xf
	s_nop 0
	s_nop 1
	v_fmac_f32_dpp v67, v67, v65 row_shr:8 row_mask:0xf bank_mask:0xf
	s_nop 1
	v_mul_f32_dpp v65, v65, v65 row_shr:8 row_mask:0xf bank_mask:0xf
	ds_read2_b32 v[48:49], v48 offset1:1
	s_waitcnt lgkmcnt(0)
	v_fmamk_f32 v48, v57, 0xbfb8aa3b, v48
	s_nop 0
	v_exp_f32_e32 v48, v48
	v_fmamk_f32 v49, v53, 0xbfb8aa3b, v49
	ds_read_b32 v53, v150 offset:1276
	s_nop 0
	v_add_f32_e32 v48, 1.0, v48
	v_rcp_f32_e32 v48, v48
	v_exp_f32_e32 v49, v49
	s_waitcnt lgkmcnt(0)
	v_mul_f32_e32 v48, v53, v48
	v_exp_f32_e32 v64, v48
	v_add_f32_e32 v49, 1.0, v49
	v_rcp_f32_e32 v49, v49
	v_fma_f32 v48, -v64, v64, 1.0
	v_max_f32_e32 v48, 0, v48
	v_sqrt_f32_e32 v48, v48
	v_mul_f32_e32 v49, v49, v52
	v_mov_b32_e32 v52, v65
	v_mul_f32_e32 v66, v49, v48
	s_nop 1
	v_fmac_f32_dpp v66, v66, v64 row_shr:1 row_mask:0xf bank_mask:0xf
	s_nop 1
	v_mul_f32_dpp v64, v64, v64 row_shr:1 row_mask:0xf bank_mask:0xf
	s_nop 0
	s_nop 1
	v_fmac_f32_dpp v66, v66, v64 row_shr:2 row_mask:0xf bank_mask:0xf
	s_nop 1
	v_mul_f32_dpp v64, v64, v64 row_shr:2 row_mask:0xf bank_mask:0xf
	s_nop 0
	s_nop 1
	v_fmac_f32_dpp v66, v66, v64 row_shr:4 row_mask:0xf bank_mask:0xf
	s_nop 1
	v_mul_f32_dpp v64, v64, v64 row_shr:4 row_mask:0xf bank_mask:0xf
	s_nop 0
	s_nop 1
	v_fmac_f32_dpp v66, v66, v64 row_shr:8 row_mask:0xf bank_mask:0xf
	s_nop 1
	v_mul_f32_dpp v64, v64, v64 row_shr:8 row_mask:0xf bank_mask:0xf
	s_nop 0
	v_pk_fma_f32 v[48:49], v[116:117], v[64:65], v[66:67]
	v_mov_b32_e32 v53, v64
	v_pk_mov_b32 v[64:65], v[48:49], v[48:49] op_sel:[1,0]
	ds_bpermute_b32 v117, v149, v49
	v_pk_mul_f32 v[56:57], v[124:125], v[52:53]
	ds_bpermute_b32 v116, v149, v48
	v_cvt_pk_bf16_f32 v52, v62, v63
	v_cvt_pk_bf16_f32 v53, v60, v61
	v_cvt_pk_bf16_f32 v55, v64, v65
	v_lshl_add_u64 v[48:49], s[6:7], 0, v[10:11]
	ds_bpermute_b32 v124, v149, v56
	ds_bpermute_b32 v125, v149, v57
	global_store_dwordx4 v[48:49], v[52:55], off
	v_cvt_pk_bf16_f32 v48, v58, v59
	v_cvt_pk_bf16_f32 v49, v46, v47
	v_cvt_pk_bf16_f32 v51, v56, v57
	v_lshl_add_u64 v[10:11], s[18:19], 0, v[10:11]
	global_store_dwordx4 v[10:11], v[48:51], off
	s_waitcnt vmcnt(5)
	v_mov_b64_e32 v[52:53], v[40:41]
	v_mov_b64_e32 v[56:57], v[36:37]
	s_waitcnt vmcnt(4)
	v_mov_b64_e32 v[48:49], v[44:45]
	v_mov_b64_e32 v[60:61], v[32:33]
	v_mov_b64_e32 v[64:65], v[28:29]
	v_mov_b64_e32 v[68:69], v[24:25]
	v_mov_b64_e32 v[46:47], v[42:43]
	v_mov_b64_e32 v[50:51], v[38:39]
	v_mov_b64_e32 v[54:55], v[34:35]
	v_mov_b64_e32 v[58:59], v[30:31]
	v_mov_b64_e32 v[62:63], v[26:27]
	v_mov_b64_e32 v[66:67], v[22:23]
	s_cbranch_scc0 .LBB0_178
; __device__ __forceinline__ void rec1_unit(KArgs args, int L, int unit, LAS unsigned char* lds, int wave, int lane) {
;     ...
;     if (fr == 0) {
; #pragma unroll
;         for (int kk = 0; kk < 2; ++kk)
; #pragma unroll
;             for (int e = 0; e < 8; ++e) { const int c = 64 * hb + 32 * kk + 8 * q + e; float* ap = agg + ((size_t)(b * 16 + chk) * 512 + c) * 2; ap[0] = Acar[kk][e]; ap[1] = Hcar[kk][e]; }
;     }
	s_and_saveexec_b64 s[0:1], vcc
	s_cbranch_execz .LBB0_174
	s_ashr_i32 s11, s10, 31
	s_lshl_b64 s[4:5], s[10:11], 12
	s_add_u32 s4, s23, s4
	s_addc_u32 s5, s25, s5
	v_lshl_add_u64 v[2:3], s[4:5], 0, v[84:85]
	v_mov_b32_e32 v10, v13
	v_mov_b32_e32 v11, v7
	v_mov_b32_e32 v13, v6
	global_store_dwordx4 v[2:3], v[10:13], off
	v_lshl_add_u64 v[2:3], s[4:5], 0, v[86:87]
	v_mov_b32_e32 v6, v9
	v_mov_b32_e32 v7, v139
	v_mov_b32_e32 v9, v138
	global_store_dwordx4 v[2:3], v[6:9], off
	v_mov_b32_e32 v2, v5
	v_mov_b32_e32 v3, v135
	v_lshl_add_u64 v[6:7], s[4:5], 0, v[88:89]
	v_mov_b32_e32 v5, v134
	global_store_dwordx4 v[6:7], v[2:5], off
	v_lshl_add_u64 v[6:7], s[4:5], 0, v[90:91]
	s_nop 0
	v_mov_b32_e32 v2, v136
	v_mov_b32_e32 v3, v129
	v_mov_b32_e32 v4, v137
	v_mov_b32_e32 v5, v128
	global_store_dwordx4 v[6:7], v[2:5], off
	v_lshl_add_u64 v[6:7], s[4:5], 0, v[92:93]
	s_nop 0
	v_mov_b32_e32 v2, v132
	v_mov_b32_e32 v3, v123
	v_mov_b32_e32 v4, v133
	v_mov_b32_e32 v5, v122
	global_store_dwordx4 v[6:7], v[2:5], off
	v_lshl_add_u64 v[6:7], s[4:5], 0, v[94:95]
	s_nop 0
	v_mov_b32_e32 v2, v130
	v_mov_b32_e32 v3, v121
	v_mov_b32_e32 v4, v131
	v_mov_b32_e32 v5, v120
	global_store_dwordx4 v[6:7], v[2:5], off
	v_lshl_add_u64 v[6:7], s[4:5], 0, v[96:97]
	s_nop 0
	v_mov_b32_e32 v2, v126
	v_mov_b32_e32 v3, v119
	v_mov_b32_e32 v4, v127
	v_mov_b32_e32 v5, v118
	global_store_dwordx4 v[6:7], v[2:5], off
	v_lshl_add_u64 v[6:7], s[4:5], 0, v[98:99]
	s_waitcnt lgkmcnt(1)
	v_mov_b32_e32 v2, v124
	v_mov_b32_e32 v3, v117
	s_waitcnt lgkmcnt(0)
	v_mov_b32_e32 v4, v125
	v_mov_b32_e32 v5, v116
	global_store_dwordx4 v[6:7], v[2:5], off
	s_branch .LBB0_174
